# speedup vs baseline: 1.0425x; 1.0182x over previous
.Lprep_m3_skip:
	s_cmp_lg_u32 s2, 0
	s_cbranch_scc1 .Lprep_noslot
	s_add_u32 s54, s14, 0xe3a0100
	s_addc_u32 s55, s15, 0
	v_mov_b32_e32 v114, s6
	v_mov_b32_e32 v115, s7
	v_mov_b32_e32 v116, s12
	v_mov_b32_e32 v117, s13
	v_mov_b32_e32 v118, 0
	global_store_dwordx4 v118, v[114:117], s[54:55] sc0 sc1

.LBB0_37:
	s_or_b64 exec, exec, s[6:7]
	s_and_b64 s[6:7], s[38:39], exec
	s_cselect_b32 s3, s18, s34
	s_cselect_b32 s12, s19, s35
	s_and_b64 s[6:7], s[36:37], exec
	s_cselect_b32 s15, s15, s12
	s_cselect_b32 s14, s14, s3
	v_lshl_add_u64 v[62:63], v[62:63], 1, s[14:15]
	v_lshlrev_b64 v[64:65], 7, v[64:65]
	v_lshl_add_u64 v[62:63], v[62:63], 0, v[64:65]
	v_cndmask_b32_e64 v64, 0, 1, s[8:9]
	s_waitcnt lgkmcnt(0)
	v_cndmask_b32_e64 v69, v69, v74, s[4:5]
	v_cndmask_b32_e64 v68, v68, v73, s[4:5]
	v_cndmask_b32_e64 v67, v74, v67, s[4:5]
	v_cndmask_b32_e64 v66, v73, v66, s[4:5]
	v_cmp_ne_u32_e64 s[6:7], 1, v64
	s_andn2_b64 vcc, exec, s[8:9]
	global_store_dwordx4 v[62:63], v[66:69], off sc0 sc1
	s_cbranch_vccnz .LBB0_39
	v_cvt_pk_f16_f32 v62, v54, v55
	v_cvt_pk_f16_f32 v63, v56, v57
	v_cvt_pk_f16_f32 v64, v50, v51
	v_cvt_pk_f16_f32 v65, v52, v53
	s_cbranch_execz .LBB0_40
	s_branch .LBB0_41

.LBB0_45:
	s_or_b64 exec, exec, s[8:9]
	v_lshl_add_u64 v[50:51], v[50:51], 1, s[14:15]
	v_lshlrev_b64 v[52:53], 7, v[54:55]
	s_waitcnt lgkmcnt(0)
	v_cndmask_b32_e64 v65, v65, v57, s[4:5]
	v_cndmask_b32_e64 v64, v64, v56, s[4:5]
	v_cndmask_b32_e64 v63, v57, v63, s[4:5]
	v_cndmask_b32_e64 v62, v56, v62, s[4:5]
	v_lshl_add_u64 v[50:51], v[50:51], 0, v[52:53]
	s_and_b64 vcc, exec, s[6:7]
	global_store_dwordx4 v[50:51], v[62:65], off sc0 sc1
	s_cbranch_vccnz .LBB0_47
	v_cvt_pk_f16_f32 v50, v46, v47
	v_cvt_pk_f16_f32 v51, v48, v49
	v_cvt_pk_f16_f32 v52, v42, v43
	v_cvt_pk_f16_f32 v53, v44, v45
	s_cbranch_execz .LBB0_48
	s_branch .LBB0_49

.LBB0_53:
	s_or_b64 exec, exec, s[8:9]
	v_lshl_add_u64 v[42:43], v[42:43], 1, s[14:15]
	v_lshlrev_b64 v[44:45], 7, v[46:47]
	s_waitcnt lgkmcnt(0)
	v_cndmask_b32_e64 v53, v53, v49, s[4:5]
	v_cndmask_b32_e64 v52, v52, v48, s[4:5]
	v_cndmask_b32_e64 v51, v49, v51, s[4:5]
	v_cndmask_b32_e64 v50, v48, v50, s[4:5]
	v_lshl_add_u64 v[42:43], v[42:43], 0, v[44:45]
	s_and_b64 vcc, exec, s[6:7]
	global_store_dwordx4 v[42:43], v[50:53], off sc0 sc1
	s_cbranch_vccnz .LBB0_55
	v_cvt_pk_f16_f32 v42, v38, v39
	v_cvt_pk_f16_f32 v43, v40, v41
	v_cvt_pk_f16_f32 v44, v34, v35
	v_cvt_pk_f16_f32 v45, v36, v37
	s_cbranch_execz .LBB0_56
	s_branch .LBB0_57

.LBB0_61:
	s_or_b64 exec, exec, s[8:9]
	v_lshl_add_u64 v[34:35], v[34:35], 1, s[14:15]
	v_lshlrev_b64 v[36:37], 7, v[38:39]
	s_waitcnt lgkmcnt(0)
	v_cndmask_b32_e64 v45, v45, v41, s[4:5]
	v_cndmask_b32_e64 v44, v44, v40, s[4:5]
	v_cndmask_b32_e64 v43, v41, v43, s[4:5]
	v_cndmask_b32_e64 v42, v40, v42, s[4:5]
	v_lshl_add_u64 v[34:35], v[34:35], 0, v[36:37]
	s_and_b64 vcc, exec, s[6:7]
	global_store_dwordx4 v[34:35], v[42:45], off sc0 sc1
	s_cbranch_vccnz .LBB0_63
	v_cvt_pk_f16_f32 v34, v30, v31
	v_cvt_pk_f16_f32 v35, v32, v33
	v_cvt_pk_f16_f32 v36, v26, v27
	v_cvt_pk_f16_f32 v37, v28, v29
	s_cbranch_execz .LBB0_64
	s_branch .LBB0_65

.LBB0_69:
	s_or_b64 exec, exec, s[8:9]
	v_lshl_add_u64 v[26:27], v[26:27], 1, s[14:15]
	v_lshlrev_b64 v[28:29], 7, v[30:31]
	s_waitcnt lgkmcnt(0)
	v_cndmask_b32_e64 v37, v37, v33, s[4:5]
	v_cndmask_b32_e64 v36, v36, v32, s[4:5]
	v_cndmask_b32_e64 v35, v33, v35, s[4:5]
	v_cndmask_b32_e64 v34, v32, v34, s[4:5]
	v_lshl_add_u64 v[26:27], v[26:27], 0, v[28:29]
	s_and_b64 vcc, exec, s[6:7]
	global_store_dwordx4 v[26:27], v[34:37], off sc0 sc1
	s_cbranch_vccnz .LBB0_71
	v_cvt_pk_f16_f32 v26, v22, v23
	v_cvt_pk_f16_f32 v27, v24, v25
	v_cvt_pk_f16_f32 v28, v18, v19
	v_cvt_pk_f16_f32 v29, v20, v21
	s_cbranch_execz .LBB0_72
	s_branch .LBB0_73

.LBB0_77:
	s_or_b64 exec, exec, s[8:9]
	v_lshl_add_u64 v[18:19], v[18:19], 1, s[14:15]
	v_lshlrev_b64 v[20:21], 7, v[22:23]
	s_waitcnt lgkmcnt(0)
	v_cndmask_b32_e64 v29, v29, v25, s[4:5]
	v_cndmask_b32_e64 v28, v28, v24, s[4:5]
	v_cndmask_b32_e64 v27, v25, v27, s[4:5]
	v_cndmask_b32_e64 v26, v24, v26, s[4:5]
	v_lshl_add_u64 v[18:19], v[18:19], 0, v[20:21]
	s_and_b64 vcc, exec, s[6:7]
	global_store_dwordx4 v[18:19], v[26:29], off sc0 sc1
	s_cbranch_vccnz .LBB0_79
	v_cvt_pk_f16_f32 v18, v10, v11
	v_cvt_pk_f16_f32 v19, v12, v13
	v_cvt_pk_f16_f32 v20, v14, v15
	v_cvt_pk_f16_f32 v21, v16, v17
	s_cbranch_execz .LBB0_80
	s_branch .LBB0_81

.LBB0_85:
	s_or_b64 exec, exec, s[8:9]
	v_lshl_add_u64 v[10:11], v[10:11], 1, s[14:15]
	v_lshlrev_b64 v[12:13], 7, v[14:15]
	s_waitcnt lgkmcnt(0)
	v_cndmask_b32_e64 v21, v21, v17, s[4:5]
	v_cndmask_b32_e64 v20, v20, v16, s[4:5]
	v_cndmask_b32_e64 v19, v17, v19, s[4:5]
	v_cndmask_b32_e64 v18, v16, v18, s[4:5]
	v_lshl_add_u64 v[10:11], v[10:11], 0, v[12:13]
	s_and_b64 vcc, exec, s[6:7]
	global_store_dwordx4 v[10:11], v[18:21], off sc0 sc1
	s_cbranch_vccnz .LBB0_87
	v_cvt_pk_f16_f32 v10, v2, v3
	v_cvt_pk_f16_f32 v11, v4, v5
	s_waitcnt vmcnt(7)
	v_cvt_pk_f16_f32 v12, v6, v7
	v_cvt_pk_f16_f32 v13, v8, v9
	s_cbranch_execz .LBB0_88
	s_branch .LBB0_89

.LBB0_93:
	s_or_b64 exec, exec, s[6:7]
	v_lshl_add_u64 v[2:3], v[2:3], 1, s[14:15]
	v_lshlrev_b64 v[4:5], 7, v[6:7]
	s_waitcnt lgkmcnt(0)
	v_cndmask_b32_e64 v13, v13, v9, s[4:5]
	v_cndmask_b32_e64 v12, v12, v8, s[4:5]
	v_cndmask_b32_e64 v11, v9, v11, s[4:5]
	v_cndmask_b32_e64 v10, v8, v10, s[4:5]
	v_lshl_add_u64 v[2:3], v[2:3], 0, v[4:5]
	global_store_dwordx4 v[2:3], v[10:13], off sc0 sc1

.LBB0_108:
	s_or_b64 exec, exec, s[2:3]
	v_lshlrev_b32_e32 v32, 4, v82
	v_mov_b32_e32 v33, 0
	v_lshl_add_u64 v[0:1], s[24:25], 0, v[32:33]
	s_movk_i32 s0, 0x1000
	v_add_co_u32_e32 v0, vcc, s0, v0
	v_lshl_add_u64 v[12:13], s[26:27], 0, v[32:33]
	s_nop 0
	v_addc_co_u32_e32 v1, vcc, 0, v1, vcc
	global_load_dwordx4 v[100:103], v[0:1], off
	s_nop 0
	global_load_dwordx4 v[104:107], v32, s[24:25]
	global_load_dwordx4 v[108:111], v32, s[26:27]
	v_add_co_u32_e32 v12, vcc, s0, v12
	v_lshrrev_b32_e32 v16, 6, v82
	s_nop 0
	v_addc_co_u32_e32 v13, vcc, 0, v13, vcc
	global_load_dwordx4 v[112:115], v[12:13], off
	v_lshl_add_u32 v34, s4, 2, v16
	v_ashrrev_i32_e32 v35, 31, v34
	v_lshlrev_b64 v[16:17], 13, v[34:35]
	v_lshl_add_u64 v[16:17], s[22:23], 0, v[16:17]
	v_mbcnt_lo_u32_b32 v35, -1, 0
	v_mbcnt_hi_u32_b32 v35, -1, v35
	v_xor_b32_e32 v56, 16, v35
	v_xor_b32_e32 v57, 8, v35
	v_xor_b32_e32 v58, 4, v35
	s_mov_b32 s2, 0x800000
	s_movk_i32 s3, 0x1080
	v_mov_b32_e32 v116, v32
	v_and_b32_e32 v32, 0x3f0, v32
	v_lshl_add_u64 v[0:1], v[16:17], 0, v[32:33]
	global_load_dwordx4 v[28:31], v[0:1], off sc0 sc1 nt
	global_load_dwordx4 v[24:27], v[0:1], off offset:1024 sc0 sc1 nt
	global_load_dwordx4 v[20:23], v[0:1], off offset:2048 sc0 sc1 nt
	global_load_dwordx4 v[16:19], v[0:1], off offset:3072 sc0 sc1 nt
	v_add_co_u32_e32 v36, vcc, s0, v0
	s_nop 1
	v_addc_co_u32_e32 v37, vcc, 0, v1, vcc
	global_load_dwordx4 v[12:15], v[36:37], off sc0 sc1 nt
	global_load_dwordx4 v[8:11], v[36:37], off offset:1024 sc0 sc1 nt
	global_load_dwordx4 v[4:7], v[36:37], off offset:2048 sc0 sc1 nt
	global_load_dwordx4 v[0:3], v[36:37], off offset:3072 sc0 sc1 nt
	s_waitcnt vmcnt(8)
	ds_write_b128 v116, v[104:107]
	ds_write_b128 v116, v[108:111] offset:8192
	ds_write_b128 v116, v[100:103] offset:4096
	ds_write_b128 v116, v[112:115] offset:12288
	s_waitcnt vmcnt(7)
	v_mov_b32_e32 v38, v29
	v_and_b32_e32 v36, 64, v35
	v_xor_b32_e32 v37, 32, v35
	v_add_u32_e32 v59, 64, v36
	v_cmp_lt_i32_e32 vcc, v37, v59
	s_waitcnt vmcnt(6)
	v_mov_b32_e32 v39, v25
	v_mov_b32_e32 v40, v30
	v_cndmask_b32_e32 v36, v35, v37, vcc
	v_lshlrev_b32_e32 v83, 2, v36
	v_mov_b32_e32 v36, v28
	v_mov_b32_e32 v37, v24
	v_mov_b32_e32 v41, v26
	v_mov_b32_e32 v42, v31
	v_mov_b32_e32 v43, v27
	s_waitcnt vmcnt(5)
	v_mov_b32_e32 v44, v21
	v_mov_b32_e32 v45, v22
	v_mov_b32_e32 v46, v20
	v_mov_b32_e32 v47, v23
	v_pk_add_f32 v[36:37], v[36:37], v[38:39]
	v_pk_add_f32 v[38:39], v[40:41], v[42:43]
	v_pk_add_f32 v[40:41], v[44:45], v[46:47]
	v_pk_add_f32 v[36:37], v[36:37], v[38:39]
	v_pk_add_f32 v[38:39], v[40:41], v[40:41] op_sel:[0,1] op_sel_hi:[1,0]
	v_add_f32_e32 v36, 0, v36
	s_waitcnt vmcnt(4)
	v_add_f32_e32 v48, v16, v17
	v_add_f32_e32 v50, v18, v19
	v_add_f32_e32 v42, v36, v37
	v_cmp_lt_i32_e32 vcc, v56, v59
	s_waitcnt lgkmcnt(0)
	s_barrier
	s_waitcnt vmcnt(3)
	v_mov_b32_e32 v43, v12
	v_mov_b32_e32 v49, v14
	v_mov_b32_e32 v51, v15
	v_mov_b32_e32 v39, v13
	s_waitcnt vmcnt(2)
	v_mov_b32_e32 v44, v9
	v_mov_b32_e32 v45, v10
	v_mov_b32_e32 v46, v8
	v_mov_b32_e32 v47, v11
	v_pk_add_f32 v[40:41], v[48:49], v[50:51]
	v_pk_add_f32 v[36:37], v[42:43], v[38:39]
	v_pk_add_f32 v[44:45], v[44:45], v[46:47]
	v_pk_add_f32 v[36:37], v[36:37], v[40:41]
	v_pk_add_f32 v[44:45], v[44:45], v[44:45] op_sel:[0,1] op_sel_hi:[1,0]
	v_pk_add_f32 v[36:37], v[36:37], v[36:37] op_sel:[0,1] op_sel_hi:[1,0]
	s_waitcnt vmcnt(1)
	v_add_f32_e32 v52, v4, v5
	v_add_f32_e32 v54, v6, v7
	s_waitcnt vmcnt(0)
	v_mov_b32_e32 v53, v2
	v_mov_b32_e32 v55, v3
	v_mov_b32_e32 v45, v1
	v_mov_b32_e32 v37, v0
	v_pk_add_f32 v[46:47], v[52:53], v[54:55]
	v_pk_add_f32 v[36:37], v[36:37], v[44:45]
	v_cndmask_b32_e32 v39, v35, v56, vcc
	v_pk_add_f32 v[36:37], v[36:37], v[46:47]
	v_lshlrev_b32_e32 v93, 2, v39
	v_add_f32_e32 v36, v36, v37
	ds_bpermute_b32 v37, v83, v36
	v_cmp_lt_i32_e32 vcc, v57, v59
	v_xor_b32_e32 v38, 2, v35
	v_xor_b32_e32 v39, 1, v35
	v_cndmask_b32_e32 v40, v35, v57, vcc
	s_waitcnt lgkmcnt(0)
	v_add_f32_e32 v36, v36, v37
	ds_bpermute_b32 v37, v93, v36
	v_lshlrev_b32_e32 v96, 2, v40
	v_cmp_lt_i32_e32 vcc, v58, v59
	v_mov_b32_e32 v46, v22
	v_mov_b32_e32 v56, v28
	s_waitcnt lgkmcnt(0)
	v_add_f32_e32 v36, v36, v37
	ds_bpermute_b32 v37, v96, v36
	v_cndmask_b32_e32 v40, v35, v58, vcc
	v_lshlrev_b32_e32 v97, 2, v40
	v_cmp_lt_i32_e32 vcc, v38, v59
	v_mov_b32_e32 v40, v10
	s_waitcnt lgkmcnt(0)
	v_add_f32_e32 v36, v36, v37
	ds_bpermute_b32 v37, v97, v36
	v_cndmask_b32_e32 v38, v35, v38, vcc
	v_lshlrev_b32_e32 v98, 2, v38
	v_cmp_lt_i32_e32 vcc, v39, v59
	v_mov_b32_e32 v58, v24
	s_waitcnt lgkmcnt(0)
	v_add_f32_e32 v36, v36, v37
	ds_bpermute_b32 v37, v98, v36
	v_cndmask_b32_e32 v35, v35, v39, vcc
	v_lshlrev_b32_e32 v35, 2, v35
	v_mov_b32_e32 v52, v18
	v_mov_b32_e32 v48, v12
	s_waitcnt lgkmcnt(0)
	v_add_f32_e32 v37, v36, v37
	ds_bpermute_b32 v39, v35, v37
	v_mov_b32_e32 v38, v6
	v_mov_b32_e32 v36, v0
	s_waitcnt lgkmcnt(0)
	v_add_f32_e32 v44, v37, v39
	v_fmamk_f32 v63, v44, 0xba000000, v21
	v_fmamk_f32 v62, v44, 0xba000000, v20
	v_fmamk_f32 v47, v44, 0xba000000, v23
	v_fmac_f32_e32 v46, 0xba000000, v44
	v_fmamk_f32 v51, v44, 0xba000000, v9
	v_fmamk_f32 v50, v44, 0xba000000, v8
	v_fmamk_f32 v41, v44, 0xba000000, v11
	v_fmac_f32_e32 v40, 0xba000000, v44
	v_fmamk_f32 v57, v44, 0xba000000, v29
	v_fmamk_f32 v59, v44, 0xba000000, v25
	v_fmamk_f32 v65, v44, 0xba000000, v31
	v_fmamk_f32 v67, v44, 0xba000000, v27
	v_fmac_f32_e32 v56, 0xba000000, v44
	v_fmac_f32_e32 v58, 0xba000000, v44
	v_fmamk_f32 v64, v44, 0xba000000, v30
	v_fmamk_f32 v66, v44, 0xba000000, v26
	v_pk_mul_f32 v[68:69], v[46:47], v[46:47]
	v_pk_mul_f32 v[70:71], v[62:63], v[62:63]
	v_pk_mul_f32 v[72:73], v[40:41], v[40:41]
	v_pk_mul_f32 v[74:75], v[50:51], v[50:51]
	v_mov_b32_e32 v78, v57
	v_mov_b32_e32 v79, v59
	v_mov_b32_e32 v84, v65
	v_mov_b32_e32 v85, v67
	v_mov_b32_e32 v76, v56
	v_mov_b32_e32 v77, v58
	v_mov_b32_e32 v80, v64
	v_mov_b32_e32 v81, v66
	v_pk_mov_b32 v[94:95], v[70:71], v[68:69] op_sel:[1,0]
	v_mov_b32_e32 v71, v69
	v_pk_mov_b32 v[68:69], v[74:75], v[72:73] op_sel:[1,0]
	v_mov_b32_e32 v75, v73
	v_pk_mul_f32 v[72:73], v[78:79], v[78:79]
	v_pk_mul_f32 v[78:79], v[84:85], v[84:85]
	v_fmamk_f32 v60, v44, 0xba000000, v16
	v_fmac_f32_e32 v52, 0xba000000, v44
	v_pk_fma_f32 v[72:73], v[76:77], v[76:77], v[72:73]
	v_pk_fma_f32 v[76:77], v[80:81], v[80:81], v[78:79]
	v_fmamk_f32 v61, v44, 0xba000000, v17
	v_fmamk_f32 v53, v44, 0xba000000, v19
	v_mul_f32_e32 v86, v60, v60
	v_mul_f32_e32 v88, v52, v52
	v_pk_add_f32 v[70:71], v[94:95], v[70:71]
	v_pk_add_f32 v[72:73], v[72:73], v[76:77]
	v_fmamk_f32 v49, v44, 0xba000000, v13
	v_fmac_f32_e32 v48, 0xba000000, v44
	v_fmamk_f32 v55, v44, 0xba000000, v15
	v_fmamk_f32 v54, v44, 0xba000000, v14
	v_pk_fma_f32 v[84:85], v[60:61], v[60:61], v[86:87] op_sel_hi:[1,1,0]
	v_pk_fma_f32 v[86:87], v[52:53], v[52:53], v[88:89] op_sel_hi:[1,1,0]
	v_pk_add_f32 v[70:71], v[70:71], v[70:71] op_sel_hi:[0,1]
	v_pk_add_f32 v[72:73], v[72:73], v[72:73] op_sel_hi:[0,1]
	v_mul_f32_e32 v84, v48, v48
	v_mul_f32_e32 v86, v49, v49
	v_mul_f32_e32 v70, v54, v54
	v_mul_f32_e32 v72, v55, v55
	v_fmamk_f32 v42, v44, 0xba000000, v4
	v_fmac_f32_e32 v38, 0xba000000, v44
	v_pk_add_f32 v[68:69], v[68:69], v[74:75]
	v_pk_add_f32 v[74:75], v[84:85], v[86:87]
	v_pk_add_f32 v[70:71], v[70:71], v[72:73]
	v_fmamk_f32 v43, v44, 0xba000000, v5
	v_fmamk_f32 v39, v44, 0xba000000, v7
	v_mul_f32_e32 v90, v42, v42
	v_mul_f32_e32 v92, v38, v38
	v_pk_add_f32 v[70:71], v[74:75], v[70:71]
	v_fmamk_f32 v37, v44, 0xba000000, v1
	v_fmac_f32_e32 v36, 0xba000000, v44
	v_fmamk_f32 v45, v44, 0xba000000, v3
	v_fmamk_f32 v44, v44, 0xba000000, v2
	v_pk_fma_f32 v[88:89], v[42:43], v[42:43], v[90:91] op_sel_hi:[1,1,0]
	v_pk_fma_f32 v[90:91], v[38:39], v[38:39], v[92:93] op_sel_hi:[1,1,0]
	v_pk_add_f32 v[68:69], v[68:69], v[68:69] op_sel_hi:[0,1]
	v_pk_add_f32 v[70:71], v[70:71], v[70:71] op_sel_hi:[0,1]
	v_mul_f32_e32 v88, v36, v36
	v_mul_f32_e32 v90, v37, v37
	v_mul_f32_e32 v68, v44, v44
	v_mul_f32_e32 v70, v45, v45
	v_pk_add_f32 v[76:77], v[88:89], v[90:91]
	v_pk_add_f32 v[68:69], v[68:69], v[70:71]
	v_mov_b32_e32 v81, v33
	v_pk_add_f32 v[68:69], v[76:77], v[68:69]
	v_mov_b32_e32 v70, 0x3727c5ac
	v_add_f32_e32 v68, v68, v69
	ds_bpermute_b32 v69, v83, v68
	v_lshlrev_b32_e32 v72, 3, v82
	v_and_b32_e32 v79, 1, v82
	v_and_b32_e32 v72, 0x1f0, v72
	v_lshl_or_b32 v80, v79, 9, v72
	s_waitcnt lgkmcnt(0)
	v_add_f32_e32 v68, v68, v69
	ds_bpermute_b32 v69, v93, v68
	v_mov_b32_e32 v78, s28
	s_waitcnt lgkmcnt(0)
	v_add_f32_e32 v69, v68, v69
	ds_bpermute_b32 v71, v96, v69
	v_mov_b32_e32 v68, s30
	s_waitcnt lgkmcnt(0)
	v_add_f32_e32 v71, v69, v71
	ds_bpermute_b32 v73, v97, v71
	v_mov_b32_e32 v69, s31
	v_mad_i64_i32 v[68:69], s[0:1], v34, s3, v[68:69]
	v_lshl_add_u64 v[68:69], v[68:69], 0, v[80:81]
	s_waitcnt lgkmcnt(0)
	v_add_f32_e32 v71, v71, v73
	ds_bpermute_b32 v73, v98, v71
	s_waitcnt lgkmcnt(0)
	v_add_f32_e32 v33, v71, v73
	ds_bpermute_b32 v71, v35, v33
	s_waitcnt lgkmcnt(0)
	v_add_f32_e32 v33, v33, v71
	v_fmac_f32_e32 v70, 0x3a000000, v33
	v_mul_f32_e32 v33, 0x4b800000, v70
	v_cmp_gt_f32_e32 vcc, s2, v70
	s_nop 1
	v_cndmask_b32_e32 v33, v70, v33, vcc
	v_rsq_f32_e32 v33, v33
	ds_read_b128 v[70:73], v32
	ds_read_b128 v[74:77], v32 offset:8192
	v_cvt_pk_f16_f32 v83, v28, v29
	v_cvt_pk_f16_f32 v84, v30, v31
	v_mul_f32_e32 v28, 0x45800000, v33
	v_cndmask_b32_e32 v82, v33, v28, vcc
	v_pk_mul_f32 v[28:29], v[56:57], v[82:83] op_sel_hi:[1,0]
	v_pk_mul_f32 v[30:31], v[64:65], v[82:83] op_sel_hi:[1,0]
	s_waitcnt lgkmcnt(0)
	v_pk_fma_f32 v[28:29], v[70:71], v[28:29], v[74:75]
	v_pk_fma_f32 v[30:31], v[72:73], v[30:31], v[76:77]
	v_pk_mul_f32 v[64:65], v[58:59], v[82:83] op_sel_hi:[1,0]
	v_cvt_pk_bf16_f32 v33, v28, v29
	v_cvt_pk_bf16_f32 v70, v30, v31
	ds_read_b128 v[28:31], v32 offset:1024
	ds_read_b128 v[56:59], v32 offset:9216
	v_pk_mul_f32 v[66:67], v[66:67], v[82:83] op_sel_hi:[1,0]
	v_cmp_eq_u32_e32 vcc, 0, v79
	v_cvt_pk_f16_f32 v71, v24, v25
	v_cvt_pk_f16_f32 v72, v26, v27
	s_waitcnt lgkmcnt(0)
	v_pk_fma_f32 v[24:25], v[30:31], v[66:67], v[58:59]
	v_pk_fma_f32 v[26:27], v[28:29], v[64:65], v[56:57]
	v_cndmask_b32_e32 v59, v83, v71, vcc
	v_cndmask_b32_e32 v64, v84, v72, vcc
	v_cvt_pk_bf16_f32 v56, v26, v27
	v_cvt_pk_bf16_f32 v57, v24, v25
	ds_read_b128 v[24:27], v32 offset:2048
	ds_read_b128 v[28:31], v32 offset:10240
	ds_bpermute_b32 v59, v35, v59
	ds_bpermute_b32 v64, v35, v64
	v_pk_mul_f32 v[62:63], v[62:63], v[82:83] op_sel_hi:[1,0]
	v_pk_mul_f32 v[46:47], v[46:47], v[82:83] op_sel_hi:[1,0]
	v_cndmask_b32_e32 v58, v70, v57, vcc
	v_cndmask_b32_e32 v65, v33, v56, vcc
	s_waitcnt lgkmcnt(2)
	v_pk_fma_f32 v[30:31], v[26:27], v[46:47], v[30:31]
	v_pk_fma_f32 v[28:29], v[24:25], v[62:63], v[28:29]
	s_waitcnt lgkmcnt(1)
	v_cndmask_b32_e32 v26, v71, v59, vcc
	v_cndmask_b32_e32 v24, v59, v83, vcc
	s_waitcnt lgkmcnt(0)
	v_cndmask_b32_e32 v27, v72, v64, vcc
	v_cndmask_b32_e32 v25, v64, v84, vcc
	global_store_dwordx4 v[68:69], v[24:27], off sc0 sc1
	ds_bpermute_b32 v24, v35, v65
	ds_bpermute_b32 v25, v35, v58
	v_mov_b32_e32 v79, s29
	v_mad_i64_i32 v[46:47], s[0:1], v34, s3, v[78:79]
	s_waitcnt lgkmcnt(1)
	v_cndmask_b32_e32 v26, v56, v24, vcc
	v_cndmask_b32_e32 v24, v24, v33, vcc
	s_waitcnt lgkmcnt(0)
	v_cndmask_b32_e32 v27, v57, v25, vcc
	v_cndmask_b32_e32 v25, v25, v70, vcc
	v_lshl_add_u64 v[46:47], v[46:47], 0, v[80:81]
	global_store_dwordx4 v[46:47], v[24:27], off sc0 sc1
	v_cvt_pk_f16_f32 v33, v20, v21
	v_cvt_pk_f16_f32 v34, v22, v23
	v_cvt_pk_bf16_f32 v56, v28, v29
	v_cvt_pk_bf16_f32 v57, v30, v31
	ds_read_b128 v[20:23], v32 offset:3072
	ds_read_b128 v[24:27], v32 offset:11264
	v_pk_mul_f32 v[28:29], v[60:61], v[82:83] op_sel_hi:[1,0]
	v_pk_mul_f32 v[30:31], v[52:53], v[82:83] op_sel_hi:[1,0]
	s_waitcnt lgkmcnt(0)
	v_pk_fma_f32 v[20:21], v[20:21], v[28:29], v[24:25]
	v_pk_fma_f32 v[22:23], v[22:23], v[30:31], v[26:27]
	v_cvt_pk_f16_f32 v24, v16, v17
	v_cvt_pk_f16_f32 v25, v18, v19
	v_cvt_pk_bf16_f32 v16, v20, v21
	s_nop 0
	v_cvt_pk_bf16_f32 v17, v22, v23
	v_cndmask_b32_e32 v19, v56, v16, vcc
	v_cndmask_b32_e32 v18, v57, v17, vcc
	v_cndmask_b32_e32 v20, v34, v25, vcc
	v_cndmask_b32_e32 v21, v33, v24, vcc
	ds_bpermute_b32 v19, v35, v19
	ds_bpermute_b32 v22, v35, v18
	ds_bpermute_b32 v21, v35, v21
	ds_bpermute_b32 v26, v35, v20
	s_waitcnt lgkmcnt(3)
	v_cndmask_b32_e32 v18, v16, v19, vcc
	v_cndmask_b32_e32 v16, v19, v56, vcc
	s_waitcnt lgkmcnt(2)
	v_cndmask_b32_e32 v19, v17, v22, vcc
	v_cndmask_b32_e32 v17, v22, v57, vcc
	s_waitcnt lgkmcnt(1)
	v_cndmask_b32_e32 v22, v24, v21, vcc
	v_cndmask_b32_e32 v20, v21, v33, vcc
	s_waitcnt lgkmcnt(0)
	v_cndmask_b32_e32 v23, v25, v26, vcc
	v_cndmask_b32_e32 v21, v26, v34, vcc
	ds_read_b128 v[24:27], v32 offset:4096
	ds_read_b128 v[28:31], v32 offset:12288
	global_store_dwordx4 v[68:69], v[20:23], off offset:1024 sc0 sc1
	global_store_dwordx4 v[46:47], v[16:19], off offset:1024 sc0 sc1
	s_nop 0
	v_pk_mul_f32 v[20:21], v[50:51], v[82:83] op_sel_hi:[1,0]
	v_pk_mul_f32 v[16:17], v[48:49], v[82:83] op_sel_hi:[1,0]
	v_pk_mul_f32 v[18:19], v[54:55], v[82:83] op_sel_hi:[1,0]
	s_waitcnt lgkmcnt(0)
	v_pk_fma_f32 v[16:17], v[16:17], v[24:25], v[28:29]
	v_pk_fma_f32 v[18:19], v[18:19], v[26:27], v[30:31]
	v_cvt_pk_f16_f32 v24, v12, v13
	v_cvt_pk_f16_f32 v25, v14, v15
	v_cvt_pk_bf16_f32 v26, v16, v17
	v_pk_mul_f32 v[22:23], v[40:41], v[82:83] op_sel_hi:[1,0]
	v_cvt_pk_bf16_f32 v27, v18, v19
	ds_read_b128 v[12:15], v32 offset:5120
	ds_read_b128 v[16:19], v32 offset:13312
	s_waitcnt lgkmcnt(0)
	v_pk_fma_f32 v[12:13], v[20:21], v[12:13], v[16:17]
	v_pk_fma_f32 v[14:15], v[22:23], v[14:15], v[18:19]
	v_cvt_pk_f16_f32 v16, v8, v9
	v_cvt_pk_f16_f32 v17, v10, v11
	v_cvt_pk_bf16_f32 v8, v12, v13
	s_nop 0
	v_cvt_pk_bf16_f32 v9, v14, v15
	v_cndmask_b32_e32 v11, v26, v8, vcc
	v_cndmask_b32_e32 v10, v27, v9, vcc
	v_cndmask_b32_e32 v12, v25, v17, vcc
	v_cndmask_b32_e32 v13, v24, v16, vcc
	ds_bpermute_b32 v11, v35, v11
	ds_bpermute_b32 v14, v35, v10
	ds_bpermute_b32 v13, v35, v13
	ds_bpermute_b32 v18, v35, v12
	s_waitcnt lgkmcnt(3)
	v_cndmask_b32_e32 v10, v8, v11, vcc
	v_cndmask_b32_e32 v8, v11, v26, vcc
	s_waitcnt lgkmcnt(2)
	v_cndmask_b32_e32 v11, v9, v14, vcc
	v_cndmask_b32_e32 v9, v14, v27, vcc
	s_waitcnt lgkmcnt(1)
	v_cndmask_b32_e32 v14, v16, v13, vcc
	v_cndmask_b32_e32 v12, v13, v24, vcc
	s_waitcnt lgkmcnt(0)
	v_cndmask_b32_e32 v15, v17, v18, vcc
	v_cndmask_b32_e32 v13, v18, v25, vcc
	ds_read_b128 v[16:19], v32 offset:6144
	ds_read_b128 v[20:23], v32 offset:14336
	global_store_dwordx4 v[68:69], v[12:15], off offset:2048 sc0 sc1
	global_store_dwordx4 v[46:47], v[8:11], off offset:2048 sc0 sc1
	s_nop 0
	v_pk_mul_f32 v[12:13], v[36:37], v[82:83] op_sel_hi:[1,0]
	v_pk_mul_f32 v[8:9], v[42:43], v[82:83] op_sel_hi:[1,0]
	v_pk_mul_f32 v[10:11], v[38:39], v[82:83] op_sel_hi:[1,0]
	s_waitcnt lgkmcnt(0)
	v_pk_fma_f32 v[8:9], v[8:9], v[16:17], v[20:21]
	v_pk_fma_f32 v[10:11], v[10:11], v[18:19], v[22:23]
	v_cvt_pk_f16_f32 v16, v4, v5
	v_cvt_pk_f16_f32 v17, v6, v7
	v_cvt_pk_bf16_f32 v18, v8, v9
	v_pk_mul_f32 v[14:15], v[44:45], v[82:83] op_sel_hi:[1,0]
	v_cvt_pk_bf16_f32 v19, v10, v11
	ds_read_b128 v[4:7], v32 offset:7168
	ds_read_b128 v[8:11], v32 offset:15360
	s_waitcnt lgkmcnt(0)
	v_pk_fma_f32 v[4:5], v[12:13], v[4:5], v[8:9]
	v_pk_fma_f32 v[6:7], v[14:15], v[6:7], v[10:11]
	v_cvt_pk_f16_f32 v8, v0, v1
	v_cvt_pk_f16_f32 v9, v2, v3
	v_cvt_pk_bf16_f32 v0, v4, v5
	s_nop 0
	v_cvt_pk_bf16_f32 v1, v6, v7
	v_cndmask_b32_e32 v3, v18, v0, vcc
	v_cndmask_b32_e32 v2, v19, v1, vcc
	v_cndmask_b32_e32 v4, v17, v9, vcc
	v_cndmask_b32_e32 v5, v16, v8, vcc
	ds_bpermute_b32 v3, v35, v3
	ds_bpermute_b32 v6, v35, v2
	ds_bpermute_b32 v5, v35, v5
	ds_bpermute_b32 v10, v35, v4
	s_waitcnt lgkmcnt(3)
	v_cndmask_b32_e32 v2, v0, v3, vcc
	v_cndmask_b32_e32 v0, v3, v18, vcc
	s_waitcnt lgkmcnt(2)
	v_cndmask_b32_e32 v3, v1, v6, vcc
	v_cndmask_b32_e32 v1, v6, v19, vcc
	s_waitcnt lgkmcnt(1)
	v_cndmask_b32_e32 v6, v8, v5, vcc
	v_cndmask_b32_e32 v4, v5, v16, vcc
	s_waitcnt lgkmcnt(0)
	v_cndmask_b32_e32 v7, v9, v10, vcc
	v_cndmask_b32_e32 v5, v10, v17, vcc
	global_store_dwordx4 v[68:69], v[4:7], off offset:3072 sc0 sc1
	global_store_dwordx4 v[46:47], v[0:3], off offset:3072 sc0 sc1

.LBB2_25:
	s_mov_b32 s1, 0x2aaaaaab
	v_mul_hi_i32 v122, v182, s1
	v_lshrrev_b32_e32 v123, 31, v122
	v_ashrrev_i32_e32 v122, 6, v122
	v_add_u32_e32 v122, v122, v123
	v_mul_i32_i24_e32 v123, 0xfffffe80, v122
	v_add_u32_e32 v123, v123, v182
	s_movk_i32 s0, 0x80
	v_and_b32_e32 v124, 0xffffff80, v123
	v_mov_b32_e32 v128, s20
	v_mov_b32_e32 v129, s10
	v_cmp_eq_u32_e32 vcc, s0, v124
	v_mov_b32_e32 v130, s21
	v_mov_b32_e32 v131, s11
	v_or_b32_e32 v1, s7, v1
	v_cndmask_b32_e32 v124, v128, v129, vcc
	v_cndmask_b32_e32 v125, v130, v131, vcc
	v_mov_b32_e32 v132, s9
	v_cmp_gt_u32_e32 vcc, s0, v123
	v_mov_b32_e32 v133, s8
	v_ashrrev_i32_e32 v123, 31, v122
	v_lshl_add_u32 v126, s24, 5, v1
	v_mov_b32_e32 v1, 0
	v_and_b32_e32 v127, 0x78, v182
	v_cndmask_b32_e32 v125, v125, v132, vcc
	v_cndmask_b32_e32 v124, v124, v133, vcc
	v_lshlrev_b64 v[122:123], 19, v[122:123]
	v_lshl_add_u64 v[122:123], v[124:125], 0, v[122:123]
	v_lshlrev_b32_e32 v124, 1, v127
	v_mov_b32_e32 v125, v1
	v_lshl_add_u64 v[122:123], v[122:123], 0, v[124:125]
	s_waitcnt vmcnt(5)
	v_pk_add_f32 v[124:125], v[96:97], v[116:117]
	v_pk_add_f32 v[96:97], v[94:95], v[114:115]
	v_lshlrev_b32_e32 v0, 15, v0
	s_waitcnt vmcnt(4)
	v_pk_add_f32 v[88:89], v[88:89], v[120:121]
	v_pk_add_f32 v[86:87], v[86:87], v[118:119]
	v_and_b32_e32 v0, 0x8000, v0
	v_cvt_pk_bf16_f32 v94, v86, v87
	v_cvt_pk_bf16_f32 v95, v88, v89
	v_cvt_pk_bf16_f32 v96, v96, v97
	v_cvt_pk_bf16_f32 v97, v124, v125
	v_ashrrev_i32_e32 v124, 1, v126
	v_ashrrev_i32_e32 v125, 31, v124
	v_lshl_add_u64 v[86:87], v[124:125], 0, v[0:1]
	v_lshlrev_b64 v[86:87], 8, v[86:87]
	v_lshl_add_u64 v[88:89], v[122:123], 0, v[86:87]
	v_pk_add_f32 v[78:79], v[78:79], v[118:119]
	global_store_dwordx4 v[88:89], v[94:97], off sc0 sc1
	v_cvt_pk_bf16_f32 v88, v78, v79
	v_or_b32_e32 v78, 8, v124
	v_ashrrev_i32_e32 v79, 31, v78
	v_lshl_add_u64 v[78:79], v[78:79], 0, v[0:1]
	v_pk_add_f32 v[80:81], v[80:81], v[120:121]
	v_lshlrev_b64 v[78:79], 8, v[78:79]
	v_pk_add_f32 v[90:91], v[90:91], v[114:115]
	v_cvt_pk_bf16_f32 v89, v80, v81
	v_lshl_add_u64 v[80:81], v[122:123], 0, v[78:79]
	v_pk_add_f32 v[92:93], v[92:93], v[116:117]
	v_cvt_pk_bf16_f32 v90, v90, v91
	v_pk_add_f32 v[70:71], v[70:71], v[118:119]
	v_cvt_pk_bf16_f32 v91, v92, v93
	global_store_dwordx4 v[80:81], v[88:91], off sc0 sc1
	v_cvt_pk_bf16_f32 v80, v70, v71
	v_pk_add_f32 v[72:73], v[72:73], v[120:121]
	v_pk_add_f32 v[82:83], v[82:83], v[114:115]
	v_add_u32_e32 v88, 0x80, v126
	v_ashrrev_i32_e32 v70, 1, v88
	v_ashrrev_i32_e32 v71, 31, v70
	v_lshl_add_u64 v[70:71], v[70:71], 0, v[0:1]
	v_lshlrev_b64 v[70:71], 8, v[70:71]
	v_cvt_pk_bf16_f32 v81, v72, v73
	v_lshl_add_u64 v[72:73], v[122:123], 0, v[70:71]
	v_pk_add_f32 v[84:85], v[84:85], v[116:117]
	v_cvt_pk_bf16_f32 v82, v82, v83
	v_pk_add_f32 v[66:67], v[66:67], v[118:119]
	v_cvt_pk_bf16_f32 v83, v84, v85
	global_store_dwordx4 v[72:73], v[80:83], off sc0 sc1
	v_cvt_pk_bf16_f32 v72, v66, v67
	v_pk_add_f32 v[68:69], v[68:69], v[120:121]
	v_pk_add_f32 v[74:75], v[74:75], v[114:115]
	v_add_u32_e32 v80, 0x90, v126
	v_ashrrev_i32_e32 v66, 1, v80
	v_ashrrev_i32_e32 v67, 31, v66
	v_lshl_add_u64 v[66:67], v[66:67], 0, v[0:1]
	v_lshlrev_b64 v[66:67], 8, v[66:67]
	v_cvt_pk_bf16_f32 v73, v68, v69
	v_lshl_add_u64 v[68:69], v[122:123], 0, v[66:67]
	v_mul_hi_i32 v0, v180, s1
	v_pk_add_f32 v[76:77], v[76:77], v[116:117]
	v_cvt_pk_bf16_f32 v74, v74, v75
	s_waitcnt vmcnt(5)
	v_pk_add_f32 v[56:57], v[56:57], v[112:113]
	v_cvt_pk_bf16_f32 v75, v76, v77
	global_store_dwordx4 v[68:69], v[72:75], off sc0 sc1
	v_lshrrev_b32_e32 v68, 31, v0
	v_ashrrev_i32_e32 v0, 6, v0
	v_add_u32_e32 v68, v0, v68
	v_mul_i32_i24_e32 v0, 0xfffffe80, v68
	v_add_u32_e32 v0, v0, v180
	v_and_b32_e32 v69, 0xffffff80, v0
	v_cmp_eq_u32_e32 vcc, s0, v69
	v_and_b32_e32 v74, 0x78, v180
	v_pk_add_f32 v[54:55], v[54:55], v[110:111]
	v_cndmask_b32_e32 v69, v128, v129, vcc
	v_cndmask_b32_e32 v72, v130, v131, vcc
	v_cmp_gt_u32_e32 vcc, s0, v0
	v_lshlrev_b32_e32 v0, 1, v74
	v_pk_add_f32 v[62:63], v[62:63], v[106:107]
	v_cndmask_b32_e32 v73, v72, v132, vcc
	v_cndmask_b32_e32 v72, v69, v133, vcc
	v_ashrrev_i32_e32 v69, 31, v68
	v_lshlrev_b64 v[68:69], 19, v[68:69]
	v_lshl_add_u64 v[68:69], v[72:73], 0, v[68:69]
	v_lshl_add_u64 v[68:69], v[68:69], 0, v[0:1]
	v_cvt_pk_bf16_f32 v54, v54, v55
	v_cvt_pk_bf16_f32 v55, v56, v57
	v_cvt_pk_bf16_f32 v56, v62, v63
	v_lshl_add_u64 v[62:63], v[68:69], 0, v[86:87]
	v_pk_add_f32 v[64:65], v[64:65], v[108:109]
	v_pk_add_f32 v[48:49], v[48:49], v[112:113]
	v_cvt_pk_bf16_f32 v57, v64, v65
	global_store_dwordx4 v[62:63], v[54:57], off sc0 sc1
	v_pk_add_f32 v[46:47], v[46:47], v[110:111]
	v_pk_add_f32 v[40:41], v[40:41], v[112:113]
	v_pk_add_f32 v[54:55], v[60:61], v[108:109]
	v_pk_add_f32 v[56:57], v[58:59], v[106:107]
	v_cvt_pk_bf16_f32 v46, v46, v47
	v_cvt_pk_bf16_f32 v47, v48, v49
	v_pk_add_f32 v[38:39], v[38:39], v[110:111]
	v_cvt_pk_bf16_f32 v48, v56, v57
	v_cvt_pk_bf16_f32 v49, v54, v55
	v_lshl_add_u64 v[54:55], v[68:69], 0, v[78:79]
	global_store_dwordx4 v[54:55], v[46:49], off sc0 sc1
	v_cvt_pk_bf16_f32 v38, v38, v39
	v_cvt_pk_bf16_f32 v39, v40, v41
	v_pk_add_f32 v[36:37], v[36:37], v[112:113]
	v_pk_add_f32 v[34:35], v[34:35], v[110:111]
	v_pk_add_f32 v[46:47], v[52:53], v[108:109]
	v_pk_add_f32 v[48:49], v[50:51], v[106:107]
	v_mul_hi_i32 v0, v178, s1
	v_cvt_pk_bf16_f32 v40, v48, v49
	v_cvt_pk_bf16_f32 v41, v46, v47
	v_lshl_add_u64 v[46:47], v[68:69], 0, v[70:71]
	global_store_dwordx4 v[46:47], v[38:41], off sc0 sc1
	v_cvt_pk_bf16_f32 v34, v34, v35
	v_cvt_pk_bf16_f32 v35, v36, v37
	s_waitcnt vmcnt(7)
	v_pk_add_f32 v[22:23], v[22:23], v[102:103]
	v_pk_add_f32 v[32:33], v[32:33], v[100:101]
	v_pk_add_f32 v[38:39], v[44:45], v[108:109]
	v_pk_add_f32 v[40:41], v[42:43], v[106:107]
	v_pk_add_f32 v[14:15], v[14:15], v[102:103]
	v_cvt_pk_bf16_f32 v36, v40, v41
	v_cvt_pk_bf16_f32 v37, v38, v39
	v_lshl_add_u64 v[38:39], v[68:69], 0, v[66:67]
	global_store_dwordx4 v[38:39], v[34:37], off sc0 sc1
	v_and_b32_e32 v38, 0x78, v178
	v_cvt_pk_bf16_f32 v22, v22, v23
	v_pk_add_f32 v[6:7], v[6:7], v[102:103]
	v_lshrrev_b32_e32 v34, 31, v0
	v_ashrrev_i32_e32 v0, 6, v0
	v_add_u32_e32 v34, v0, v34
	v_mul_i32_i24_e32 v0, 0xfffffe80, v34
	v_add_u32_e32 v0, v0, v178
	v_and_b32_e32 v35, 0xffffff80, v0
	v_cmp_eq_u32_e32 vcc, s0, v35
	v_pk_add_f32 v[4:5], v[4:5], v[104:105]
	s_nop 0
	v_cndmask_b32_e32 v35, v128, v129, vcc
	v_cndmask_b32_e32 v36, v130, v131, vcc
	v_cmp_gt_u32_e32 vcc, s0, v0
	v_lshlrev_b32_e32 v0, 1, v38
	s_nop 0
	v_cndmask_b32_e32 v37, v36, v132, vcc
	v_cndmask_b32_e32 v36, v35, v133, vcc
	v_ashrrev_i32_e32 v35, 31, v34
	v_lshlrev_b64 v[34:35], 19, v[34:35]
	v_lshl_add_u64 v[34:35], v[36:37], 0, v[34:35]
	v_lshl_add_u64 v[34:35], v[34:35], 0, v[0:1]
	v_pk_add_f32 v[0:1], v[24:25], v[104:105]
	v_pk_add_f32 v[24:25], v[30:31], v[98:99]
	v_cvt_pk_bf16_f32 v23, v0, v1
	v_lshl_add_u64 v[0:1], v[34:35], 0, v[86:87]
	v_cvt_pk_bf16_f32 v24, v24, v25
	v_cvt_pk_bf16_f32 v25, v32, v33
	global_store_dwordx4 v[0:1], v[22:25], off sc0 sc1
	v_pk_add_f32 v[0:1], v[16:17], v[104:105]
	v_pk_add_f32 v[16:17], v[26:27], v[98:99]
	v_cvt_pk_bf16_f32 v14, v14, v15
	v_cvt_pk_bf16_f32 v15, v0, v1
	v_lshl_add_u64 v[0:1], v[34:35], 0, v[78:79]
	v_pk_add_f32 v[22:23], v[28:29], v[100:101]
	v_cvt_pk_bf16_f32 v16, v16, v17
	s_nop 0
	v_cvt_pk_bf16_f32 v17, v22, v23
	global_store_dwordx4 v[0:1], v[14:17], off sc0 sc1
	v_pk_add_f32 v[0:1], v[8:9], v[104:105]
	v_pk_add_f32 v[8:9], v[18:19], v[98:99]
	v_cvt_pk_bf16_f32 v6, v6, v7
	v_cvt_pk_bf16_f32 v7, v0, v1
	v_lshl_add_u64 v[0:1], v[34:35], 0, v[70:71]
	v_pk_add_f32 v[14:15], v[20:21], v[100:101]
	v_cvt_pk_bf16_f32 v8, v8, v9
	s_nop 0
	v_cvt_pk_bf16_f32 v9, v14, v15
	global_store_dwordx4 v[0:1], v[6:9], off sc0 sc1
	v_pk_add_f32 v[0:1], v[2:3], v[102:103]
	v_pk_add_f32 v[2:3], v[10:11], v[98:99]
	v_cvt_pk_bf16_f32 v0, v0, v1
	v_cvt_pk_bf16_f32 v1, v4, v5
	v_lshl_add_u64 v[4:5], v[34:35], 0, v[66:67]
	v_pk_add_f32 v[6:7], v[12:13], v[100:101]
	v_cvt_pk_bf16_f32 v2, v2, v3
	s_nop 0
	v_cvt_pk_bf16_f32 v3, v6, v7
	global_store_dwordx4 v[4:5], v[0:3], off sc0 sc1
	s_endpgm
	.p2align	8

.LBB4_11:
	s_nop 0
	v_mov_b32_e32 v126, s20
	v_mov_b32_e32 v127, s21
	v_lshl_add_u64 v[122:123], v[122:123], 1, v[126:127]
	s_waitcnt vmcnt(7)
	v_cvt_f32_f16_sdwa v127, v110 dst_sel:DWORD dst_unused:UNUSED_PAD src0_sel:WORD_1
	v_cvt_f32_f16_sdwa v129, v111 dst_sel:DWORD dst_unused:UNUSED_PAD src0_sel:WORD_1
	v_cvt_f32_f16_e32 v128, v111
	v_cvt_f32_f16_e32 v126, v110
	v_pk_add_f32 v[64:65], v[64:65], v[96:97]
	v_pk_add_f32 v[62:63], v[62:63], v[94:95]
	v_pk_add_f32 v[64:65], v[64:65], v[128:129]
	v_pk_add_f32 v[62:63], v[62:63], v[126:127]
	v_add_f32_e32 v111, v64, v65
	v_add_f32_e32 v110, v62, v63
	v_add_f32_e32 v110, v110, v111
	v_add_f32_e32 v125, 0, v110
	v_mul_f32_e32 v110, v63, v63
	v_mul_f32_e32 v111, v64, v64
	v_fmac_f32_e32 v110, v62, v62
	v_fmac_f32_e32 v111, v65, v65
	v_add_f32_e32 v128, v110, v111
	v_cvt_f32_f16_sdwa v111, v112 dst_sel:DWORD dst_unused:UNUSED_PAD src0_sel:WORD_1
	v_cvt_f32_f16_sdwa v127, v113 dst_sel:DWORD dst_unused:UNUSED_PAD src0_sel:WORD_1
	v_cvt_f32_f16_e32 v126, v113
	v_cvt_f32_f16_e32 v110, v112
	v_pk_add_f32 v[60:61], v[60:61], v[92:93]
	v_pk_add_f32 v[58:59], v[58:59], v[90:91]
	v_pk_add_f32 v[112:113], v[60:61], v[126:127]
	v_pk_add_f32 v[60:61], v[58:59], v[110:111]
	v_add_f32_e32 v59, v112, v113
	v_add_f32_e32 v58, v60, v61
	v_add_f32_e32 v58, v58, v59
	v_add_f32_e32 v110, v125, v58
	v_mul_f32_e32 v58, v61, v61
	v_mul_f32_e32 v59, v112, v112
	v_fmac_f32_e32 v58, v60, v60
	v_fmac_f32_e32 v59, v113, v113
	v_add_f32_e32 v58, v58, v59
	v_add_f32_e32 v111, v128, v58
	v_cvt_pk_f16_f32 v58, v62, v63
	v_cvt_pk_f16_f32 v59, v64, v65
	v_cvt_pk_f16_f32 v60, v60, v61
	v_cvt_pk_f16_f32 v61, v112, v113
	v_lshl_add_u64 v[62:63], v[120:121], 1, v[122:123]
	global_store_dwordx4 v[62:63], v[58:61], off sc0 sc1
	v_pk_add_f32 v[52:53], v[52:53], v[96:97]
	v_pk_add_f32 v[64:65], v[50:51], v[94:95]
	s_waitcnt vmcnt(6)
	v_cvt_f32_f16_sdwa v59, v106 dst_sel:DWORD dst_unused:UNUSED_PAD src0_sel:WORD_1
	v_cvt_f32_f16_sdwa v61, v107 dst_sel:DWORD dst_unused:UNUSED_PAD src0_sel:WORD_1
	v_cvt_f32_f16_e32 v60, v107
	v_cvt_f32_f16_e32 v58, v106
	v_pk_add_f32 v[56:57], v[56:57], v[92:93]
	v_pk_add_f32 v[44:45], v[44:45], v[96:97]
	v_pk_add_f32 v[50:51], v[52:53], v[60:61]
	v_pk_add_f32 v[52:53], v[64:65], v[58:59]
	v_cvt_f32_f16_sdwa v59, v108 dst_sel:DWORD dst_unused:UNUSED_PAD src0_sel:WORD_1
	v_cvt_f32_f16_sdwa v61, v109 dst_sel:DWORD dst_unused:UNUSED_PAD src0_sel:WORD_1
	v_cvt_f32_f16_e32 v60, v109
	v_cvt_f32_f16_e32 v58, v108
	v_pk_add_f32 v[64:65], v[54:55], v[90:91]
	v_pk_add_f32 v[48:49], v[48:49], v[92:93]
	v_pk_add_f32 v[54:55], v[56:57], v[60:61]
	v_pk_add_f32 v[56:57], v[64:65], v[58:59]
	v_cvt_pk_f16_f32 v58, v52, v53
	v_cvt_pk_f16_f32 v59, v50, v51
	v_lshl_add_u64 v[64:65], v[118:119], 1, v[122:123]
	v_cvt_pk_f16_f32 v60, v56, v57
	v_cvt_pk_f16_f32 v61, v54, v55
	global_store_dwordx4 v[64:65], v[58:61], off sc0 sc1
	v_pk_add_f32 v[36:37], v[36:37], v[96:97]
	v_pk_add_f32 v[40:41], v[40:41], v[92:93]
	s_waitcnt vmcnt(5)
	v_cvt_f32_f16_sdwa v59, v102 dst_sel:DWORD dst_unused:UNUSED_PAD src0_sel:WORD_1
	v_cvt_f32_f16_sdwa v61, v103 dst_sel:DWORD dst_unused:UNUSED_PAD src0_sel:WORD_1
	v_cvt_f32_f16_e32 v60, v103
	v_cvt_f32_f16_e32 v58, v102
	v_pk_add_f32 v[102:103], v[42:43], v[94:95]
	v_pk_add_f32 v[94:95], v[34:35], v[94:95]
	v_pk_add_f32 v[42:43], v[44:45], v[60:61]
	v_pk_add_f32 v[44:45], v[102:103], v[58:59]
	v_cvt_f32_f16_sdwa v59, v104 dst_sel:DWORD dst_unused:UNUSED_PAD src0_sel:WORD_1
	v_cvt_f32_f16_sdwa v61, v105 dst_sel:DWORD dst_unused:UNUSED_PAD src0_sel:WORD_1
	v_cvt_f32_f16_e32 v60, v105
	v_cvt_f32_f16_e32 v58, v104
	v_pk_add_f32 v[102:103], v[46:47], v[90:91]
	v_pk_add_f32 v[90:91], v[38:39], v[90:91]
	v_pk_add_f32 v[46:47], v[48:49], v[60:61]
	v_pk_add_f32 v[48:49], v[102:103], v[58:59]
	v_cvt_pk_f16_f32 v58, v44, v45
	v_cvt_pk_f16_f32 v59, v42, v43
	v_lshl_add_u64 v[102:103], v[116:117], 1, v[122:123]
	v_cvt_pk_f16_f32 v60, v48, v49
	v_cvt_pk_f16_f32 v61, v46, v47
	global_store_dwordx4 v[102:103], v[58:61], off sc0 sc1
	v_pk_add_f32 v[32:33], v[32:33], v[72:73]
	v_pk_add_f32 v[30:31], v[30:31], v[70:71]
	s_waitcnt vmcnt(4)
	v_cvt_f32_f16_sdwa v59, v98 dst_sel:DWORD dst_unused:UNUSED_PAD src0_sel:WORD_1
	v_cvt_f32_f16_sdwa v61, v99 dst_sel:DWORD dst_unused:UNUSED_PAD src0_sel:WORD_1
	v_cvt_f32_f16_e32 v60, v99
	v_cvt_f32_f16_e32 v58, v98
	v_pk_add_f32 v[28:29], v[28:29], v[68:69]
	v_pk_add_f32 v[26:27], v[26:27], v[66:67]
	v_pk_add_f32 v[34:35], v[36:37], v[60:61]
	v_pk_add_f32 v[36:37], v[94:95], v[58:59]
	v_cvt_f32_f16_sdwa v59, v100 dst_sel:DWORD dst_unused:UNUSED_PAD src0_sel:WORD_1
	v_cvt_f32_f16_sdwa v61, v101 dst_sel:DWORD dst_unused:UNUSED_PAD src0_sel:WORD_1
	v_cvt_f32_f16_e32 v60, v101
	v_cvt_f32_f16_e32 v58, v100
	v_pk_add_f32 v[20:21], v[20:21], v[72:73]
	v_pk_add_f32 v[24:25], v[24:25], v[68:69]
	v_pk_add_f32 v[38:39], v[40:41], v[60:61]
	v_pk_add_f32 v[40:41], v[90:91], v[58:59]
	v_cvt_pk_f16_f32 v58, v36, v37
	v_cvt_pk_f16_f32 v59, v34, v35
	v_lshl_add_u64 v[90:91], v[114:115], 1, v[122:123]
	v_cvt_pk_f16_f32 v60, v40, v41
	v_cvt_pk_f16_f32 v61, v38, v39
	global_store_dwordx4 v[90:91], v[58:61], off sc0 sc1
	v_pk_add_f32 v[12:13], v[12:13], v[72:73]
	v_pk_add_f32 v[16:17], v[16:17], v[68:69]
	v_cvt_f32_f16_sdwa v59, v86 dst_sel:DWORD dst_unused:UNUSED_PAD src0_sel:WORD_1
	v_cvt_f32_f16_sdwa v61, v87 dst_sel:DWORD dst_unused:UNUSED_PAD src0_sel:WORD_1
	v_cvt_f32_f16_e32 v60, v87
	v_cvt_f32_f16_e32 v58, v86
	v_pk_add_f32 v[4:5], v[4:5], v[72:73]
	v_pk_add_f32 v[8:9], v[8:9], v[68:69]
	v_pk_add_f32 v[32:33], v[32:33], v[60:61]
	v_pk_add_f32 v[30:31], v[30:31], v[58:59]
	v_add_f32_e32 v59, v32, v33
	v_add_f32_e32 v58, v30, v31
	v_add_f32_e32 v58, v58, v59
	v_add_f32_e32 v86, v110, v58
	v_mul_f32_e32 v58, v31, v31
	v_mul_f32_e32 v59, v32, v32
	v_fmac_f32_e32 v58, v30, v30
	v_fmac_f32_e32 v59, v33, v33
	v_add_f32_e32 v58, v58, v59
	v_add_f32_e32 v87, v111, v58
	v_cvt_f32_f16_sdwa v59, v88 dst_sel:DWORD dst_unused:UNUSED_PAD src0_sel:WORD_1
	v_cvt_f32_f16_sdwa v61, v89 dst_sel:DWORD dst_unused:UNUSED_PAD src0_sel:WORD_1
	v_cvt_f32_f16_e32 v60, v89
	v_cvt_f32_f16_e32 v58, v88
	v_pk_add_f32 v[60:61], v[28:29], v[60:61]
	v_pk_add_f32 v[28:29], v[26:27], v[58:59]
	v_add_f32_e32 v27, v60, v61
	v_add_f32_e32 v26, v28, v29
	v_add_f32_e32 v26, v26, v27
	v_add_f32_e32 v58, v86, v26
	v_mul_f32_e32 v26, v29, v29
	v_mul_f32_e32 v27, v60, v60
	v_fmac_f32_e32 v26, v28, v28
	v_fmac_f32_e32 v27, v61, v61
	v_add_f32_e32 v26, v26, v27
	v_add_f32_e32 v59, v87, v26
	v_cvt_pk_f16_f32 v26, v30, v31
	v_cvt_pk_f16_f32 v27, v32, v33
	v_cvt_pk_f16_f32 v28, v28, v29
	v_cvt_pk_f16_f32 v29, v60, v61
	global_store_dwordx4 v[62:63], v[26:29], off offset:64 sc0 sc1
	v_pk_add_f32 v[30:31], v[18:19], v[70:71]
	s_nop 0
	v_cvt_f32_f16_sdwa v27, v82 dst_sel:DWORD dst_unused:UNUSED_PAD src0_sel:WORD_1
	v_cvt_f32_f16_sdwa v29, v83 dst_sel:DWORD dst_unused:UNUSED_PAD src0_sel:WORD_1
	v_cvt_f32_f16_e32 v28, v83
	v_cvt_f32_f16_e32 v26, v82
	v_pk_add_f32 v[18:19], v[20:21], v[28:29]
	v_pk_add_f32 v[20:21], v[30:31], v[26:27]
	v_cvt_f32_f16_sdwa v27, v84 dst_sel:DWORD dst_unused:UNUSED_PAD src0_sel:WORD_1
	v_cvt_f32_f16_sdwa v29, v85 dst_sel:DWORD dst_unused:UNUSED_PAD src0_sel:WORD_1
	v_cvt_f32_f16_e32 v28, v85
	v_cvt_f32_f16_e32 v26, v84
	v_pk_add_f32 v[30:31], v[22:23], v[66:67]
	v_pk_add_f32 v[22:23], v[24:25], v[28:29]
	v_pk_add_f32 v[24:25], v[30:31], v[26:27]
	v_cvt_pk_f16_f32 v26, v20, v21
	v_cvt_pk_f16_f32 v27, v18, v19
	v_pk_add_f32 v[30:31], v[10:11], v[70:71]
	v_cvt_pk_f16_f32 v28, v24, v25
	v_cvt_pk_f16_f32 v29, v22, v23
	global_store_dwordx4 v[64:65], v[26:29], off offset:64 sc0 sc1
	s_nop 1
	v_cvt_f32_f16_sdwa v27, v78 dst_sel:DWORD dst_unused:UNUSED_PAD src0_sel:WORD_1
	v_cvt_f32_f16_sdwa v29, v79 dst_sel:DWORD dst_unused:UNUSED_PAD src0_sel:WORD_1
	v_cvt_f32_f16_e32 v28, v79
	v_cvt_f32_f16_e32 v26, v78
	v_pk_add_f32 v[10:11], v[12:13], v[28:29]
	v_pk_add_f32 v[12:13], v[30:31], v[26:27]
	v_cvt_f32_f16_sdwa v27, v80 dst_sel:DWORD dst_unused:UNUSED_PAD src0_sel:WORD_1
	v_cvt_f32_f16_sdwa v29, v81 dst_sel:DWORD dst_unused:UNUSED_PAD src0_sel:WORD_1
	v_cvt_f32_f16_e32 v28, v81
	v_cvt_f32_f16_e32 v26, v80
	v_pk_add_f32 v[30:31], v[14:15], v[66:67]
	v_pk_add_f32 v[14:15], v[16:17], v[28:29]
	v_pk_add_f32 v[16:17], v[30:31], v[26:27]
	v_cvt_pk_f16_f32 v26, v12, v13
	v_cvt_pk_f16_f32 v27, v10, v11
	v_pk_add_f32 v[30:31], v[2:3], v[70:71]
	v_cvt_pk_f16_f32 v28, v16, v17
	v_cvt_pk_f16_f32 v29, v14, v15
	global_store_dwordx4 v[102:103], v[26:29], off offset:64 sc0 sc1
	s_waitcnt vmcnt(7)
	s_nop 0
	v_cvt_f32_f16_sdwa v27, v74 dst_sel:DWORD dst_unused:UNUSED_PAD src0_sel:WORD_1
	v_cvt_f32_f16_sdwa v29, v75 dst_sel:DWORD dst_unused:UNUSED_PAD src0_sel:WORD_1
	v_cvt_f32_f16_e32 v28, v75
	v_cvt_f32_f16_e32 v26, v74
	v_pk_add_f32 v[2:3], v[4:5], v[28:29]
	v_pk_add_f32 v[4:5], v[30:31], v[26:27]
	v_cvt_f32_f16_sdwa v27, v76 dst_sel:DWORD dst_unused:UNUSED_PAD src0_sel:WORD_1
	v_cvt_f32_f16_sdwa v29, v77 dst_sel:DWORD dst_unused:UNUSED_PAD src0_sel:WORD_1
	v_cvt_f32_f16_e32 v28, v77
	v_cvt_f32_f16_e32 v26, v76
	v_pk_add_f32 v[30:31], v[6:7], v[66:67]
	v_pk_add_f32 v[6:7], v[8:9], v[28:29]
	v_pk_add_f32 v[8:9], v[30:31], v[26:27]
	v_cvt_pk_f16_f32 v26, v4, v5
	v_cvt_pk_f16_f32 v27, v2, v3
	s_nop 0
	v_cvt_pk_f16_f32 v28, v8, v9
	v_cvt_pk_f16_f32 v29, v6, v7
	global_store_dwordx4 v[90:91], v[26:29], off offset:64 sc0 sc1
	s_nop 1
	v_lshl_add_u32 v26, v0, 2, 0
	v_mov_b32_e32 v27, 0
	ds_write_b32 v26, v27
	v_mbcnt_lo_u32_b32 v27, -1, 0
	v_mbcnt_hi_u32_b32 v28, -1, v27
	v_and_b32_e32 v29, 64, v28
	v_xor_b32_e32 v27, 16, v28
	v_add_u32_e32 v29, 64, v29
	v_cmp_lt_i32_e32 vcc, v27, v29
	v_xor_b32_e32 v30, 32, v28
	s_waitcnt lgkmcnt(0)
	v_cndmask_b32_e32 v27, v28, v27, vcc
	v_lshlrev_b32_e32 v27, 2, v27
	ds_bpermute_b32 v31, v27, v58
	ds_bpermute_b32 v32, v27, v59
	v_cmp_lt_i32_e32 vcc, v30, v29
	s_barrier
	s_waitcnt lgkmcnt(0)
	v_cndmask_b32_e32 v28, v28, v30, vcc
	v_lshlrev_b32_e32 v28, 2, v28
	v_add_f32_e32 v29, v58, v31
	v_add_f32_e32 v30, v59, v32
	ds_bpermute_b32 v31, v28, v29
	ds_bpermute_b32 v32, v28, v30
	v_cmp_gt_u32_e32 vcc, 16, v1
	v_or_b32_e32 v1, s0, v124
	v_lshl_add_u32 v1, v1, 2, 0
	s_and_saveexec_b64 s[0:1], vcc
	s_cbranch_execz .LBB4_13
	s_waitcnt lgkmcnt(1)
	v_add_f32_e32 v29, v29, v31
	s_waitcnt lgkmcnt(0)
	v_add_f32_e32 v30, v30, v32
	ds_add_f32 v1, v29
	ds_add_f32 v1, v30 offset:1024

.LBB5_25:
	s_mov_b32 s2, 0x3a000000
	s_waitcnt vmcnt(3)
	v_pk_mul_f32 v[144:145], v[214:215], s[2:3] op_sel_hi:[1,0]
	s_waitcnt vmcnt(2)
	v_pk_mul_f32 v[146:147], v[212:213], s[2:3] op_sel_hi:[1,0]
	v_mov_b32_e32 v149, v145
	v_mov_b32_e32 v148, v147
	v_mov_b32_e32 v150, v146
	v_mov_b32_e32 v151, v144
	v_pk_fma_f32 v[148:149], v[148:149], v[148:149], v[150:151] neg_lo:[1,0,0] neg_hi:[1,0,0]
	s_mov_b32 s4, 0x3727c5ac
	v_pk_add_f32 v[148:149], v[148:149], s[4:5] op_sel_hi:[1,0]
	s_mov_b32 s3, 0x800000
	v_mul_f32_e32 v144, 0x4b800000, v149
	v_cmp_gt_f32_e32 vcc, s3, v149
	v_mul_f32_e32 v146, 0x4b800000, v148
	v_cmp_gt_f32_e64 s[0:1], s3, v148
	v_cndmask_b32_e32 v144, v149, v144, vcc
	v_rsq_f32_e32 v144, v144
	v_cndmask_b32_e64 v146, v148, v146, s[0:1]
	v_rsq_f32_e32 v146, v146
	v_add_u32_e32 v157, 0x90, v204
	v_mul_f32_e32 v148, 0x45800000, v144
	v_cndmask_b32_e32 v156, v144, v148, vcc
	v_mul_f32_e32 v144, 0x45800000, v146
	v_cndmask_b32_e64 v152, v146, v144, s[0:1]
	v_mul_f32_e32 v158, v145, v156
	v_mul_f32_e32 v154, v147, v152
	s_waitcnt vmcnt(1)
	v_pk_mul_f32 v[144:145], v[210:211], s[2:3] op_sel_hi:[1,0]
	s_waitcnt vmcnt(0)
	v_pk_mul_f32 v[146:147], v[208:209], s[2:3] op_sel_hi:[1,0]
	v_mov_b32_e32 v149, v145
	v_mov_b32_e32 v148, v147
	v_mov_b32_e32 v150, v146
	v_mov_b32_e32 v151, v144
	v_pk_fma_f32 v[148:149], v[148:149], v[148:149], v[150:151] neg_lo:[1,0,0] neg_hi:[1,0,0]
	v_pk_mul_f32 v[164:165], v[140:141], v[158:159] op_sel_hi:[1,0]
	v_pk_add_f32 v[148:149], v[148:149], s[4:5] op_sel_hi:[1,0]
	v_pk_mul_f32 v[162:163], v[142:143], v[158:159] op_sel_hi:[1,0]
	v_mul_f32_e32 v144, 0x4b800000, v149
	v_cmp_gt_f32_e32 vcc, s3, v149
	v_mul_f32_e32 v146, 0x4b800000, v148
	v_cmp_gt_f32_e64 s[0:1], s3, v148
	v_cndmask_b32_e32 v144, v149, v144, vcc
	v_rsq_f32_e32 v144, v144
	v_cndmask_b32_e64 v146, v148, v146, s[0:1]
	v_rsq_f32_e32 v146, v146
	v_pk_fma_f32 v[124:125], v[124:125], v[156:157], v[164:165] op_sel_hi:[1,0,1] neg_lo:[0,0,1] neg_hi:[0,0,1]
	v_mul_f32_e32 v148, 0x45800000, v144
	v_cndmask_b32_e32 v148, v144, v148, vcc
	v_pk_fma_f32 v[126:127], v[126:127], v[156:157], v[162:163] op_sel_hi:[1,0,1] neg_lo:[0,0,1] neg_hi:[0,0,1]
	v_pk_add_f32 v[162:163], v[136:137], v[124:125]
	v_mul_f32_e32 v150, v145, v148
	v_mul_f32_e32 v144, 0x45800000, v146
	v_mul_f32_e32 v125, v162, v162
	v_mov_b32_e32 v124, 0xc0135761
	v_mul_f32_e32 v145, v163, v163
	v_cndmask_b32_e64 v144, v146, v144, s[0:1]
	v_fmamk_f32 v125, v125, 0xbdd2d3e8, v124
	v_fmamk_f32 v145, v145, 0xbdd2d3e8, v124
	v_pk_add_f32 v[126:127], v[138:139], v[126:127]
	v_mul_f32_e32 v146, v147, v144
	v_mul_f32_e32 v125, v162, v125
	v_mul_f32_e32 v145, v163, v145
	v_mul_f32_e32 v147, v126, v126
	v_mul_f32_e32 v149, v127, v127
	v_exp_f32_e32 v125, v125
	v_exp_f32_e32 v145, v145
	v_fmamk_f32 v147, v147, 0xbdd2d3e8, v124
	v_fmamk_f32 v149, v149, 0xbdd2d3e8, v124
	v_mul_f32_e32 v147, v126, v147
	v_mul_f32_e32 v149, v127, v149
	v_exp_f32_e32 v147, v147
	v_exp_f32_e32 v149, v149
	v_add_f32_e32 v125, 1.0, v125
	v_add_f32_e32 v145, 1.0, v145
	v_rcp_f32_e32 v125, v125
	v_rcp_f32_e32 v145, v145
	v_add_f32_e32 v147, 1.0, v147
	v_add_f32_e32 v149, 1.0, v149
	v_rcp_f32_e32 v147, v147
	v_rcp_f32_e32 v149, v149
	v_mul_f32_e32 v125, v162, v125
	v_mul_f32_e32 v145, v163, v145
	v_pk_mul_f32 v[162:163], v[132:133], v[158:159] op_sel_hi:[1,0]
	v_mul_f32_e32 v147, v126, v147
	v_pk_fma_f32 v[120:121], v[120:121], v[156:157], v[162:163] op_sel_hi:[1,0,1] neg_lo:[0,0,1] neg_hi:[0,0,1]
	v_mul_f32_e32 v149, v127, v149
	v_pk_mul_f32 v[126:127], v[134:135], v[158:159] op_sel_hi:[1,0]
	v_pk_add_f32 v[120:121], v[128:129], v[120:121]
	v_pk_fma_f32 v[122:123], v[122:123], v[156:157], v[126:127] op_sel_hi:[1,0,1] neg_lo:[0,0,1] neg_hi:[0,0,1]
	v_mul_f32_e32 v126, v120, v120
	v_mul_f32_e32 v127, v121, v121
	v_fmamk_f32 v126, v126, 0xbdd2d3e8, v124
	v_fmamk_f32 v127, v127, 0xbdd2d3e8, v124
	v_pk_add_f32 v[122:123], v[130:131], v[122:123]
	v_mul_f32_e32 v126, v120, v126
	v_mul_f32_e32 v127, v121, v127
	v_mul_f32_e32 v151, v122, v122
	v_mul_f32_e32 v159, v123, v123
	v_exp_f32_e32 v126, v126
	v_exp_f32_e32 v127, v127
	v_fmamk_f32 v151, v151, 0xbdd2d3e8, v124
	v_fmamk_f32 v159, v159, 0xbdd2d3e8, v124
	v_mul_f32_e32 v151, v122, v151
	v_mul_f32_e32 v159, v123, v159
	v_exp_f32_e32 v151, v151
	v_exp_f32_e32 v159, v159
	v_add_f32_e32 v126, 1.0, v126
	v_add_f32_e32 v127, 1.0, v127
	v_rcp_f32_e32 v126, v126
	v_rcp_f32_e32 v127, v127
	v_add_f32_e32 v151, 1.0, v151
	v_add_f32_e32 v159, 1.0, v159
	v_rcp_f32_e32 v151, v151
	v_rcp_f32_e32 v159, v159
	s_add_i32 s0, s9, 64
	v_mul_f32_e32 v120, v120, v126
	v_mul_f32_e32 v121, v121, v127
	v_cvt_pk_f16_f32 v162, v125, v145
	v_cvt_pk_f16_f32 v163, v147, v149
	v_cvt_pk_f16_f32 v164, v120, v121
	v_mad_i64_i32 v[120:121], s[2:3], v204, s0, 0
	v_lshl_add_u64 v[160:161], v[206:207], 1, s[6:7]
	v_mul_f32_e32 v122, v122, v151
	v_mul_f32_e32 v123, v123, v159
	v_lshlrev_b64 v[120:121], 1, v[120:121]
	v_add_u32_e32 v155, 0x80, v204
	v_cvt_pk_f16_f32 v165, v122, v123
	v_lshl_add_u64 v[122:123], v[160:161], 0, v[120:121]
	v_or_b32_e32 v153, 16, v204
	global_store_dwordx4 v[122:123], v[162:165], off sc0 sc1
	v_pk_mul_f32 v[122:123], v[142:143], v[154:155] op_sel_hi:[1,0]
	v_pk_mul_f32 v[126:127], v[140:141], v[154:155] op_sel_hi:[1,0]
	v_pk_fma_f32 v[114:115], v[114:115], v[152:153], v[122:123] op_sel_hi:[1,0,1] neg_lo:[0,0,1] neg_hi:[0,0,1]
	v_pk_fma_f32 v[112:113], v[112:113], v[152:153], v[126:127] op_sel_hi:[1,0,1] neg_lo:[0,0,1] neg_hi:[0,0,1]
	v_pk_add_f32 v[114:115], v[138:139], v[114:115]
	v_pk_add_f32 v[112:113], v[136:137], v[112:113]
	v_mul_f32_e32 v125, v114, v114
	v_mul_f32_e32 v122, v112, v112
	v_mul_f32_e32 v123, v113, v113
	v_mul_f32_e32 v126, v115, v115
	v_fmamk_f32 v122, v122, 0xbdd2d3e8, v124
	v_fmamk_f32 v123, v123, 0xbdd2d3e8, v124
	v_fmamk_f32 v125, v125, 0xbdd2d3e8, v124
	v_fmamk_f32 v126, v126, 0xbdd2d3e8, v124
	v_mul_f32_e32 v122, v112, v122
	v_mul_f32_e32 v123, v113, v123
	v_mul_f32_e32 v125, v114, v125
	v_mul_f32_e32 v126, v115, v126
	v_exp_f32_e32 v122, v122
	v_exp_f32_e32 v123, v123
	v_exp_f32_e32 v125, v125
	v_exp_f32_e32 v126, v126
	v_add_f32_e32 v122, 1.0, v122
	v_add_f32_e32 v123, 1.0, v123
	v_add_f32_e32 v125, 1.0, v125
	v_add_f32_e32 v126, 1.0, v126
	v_rcp_f32_e32 v122, v122
	v_rcp_f32_e32 v123, v123
	v_rcp_f32_e32 v125, v125
	v_rcp_f32_e32 v126, v126
	v_mul_f32_e32 v122, v112, v122
	v_mul_f32_e32 v123, v113, v123
	v_mul_f32_e32 v125, v114, v125
	v_mul_f32_e32 v126, v115, v126
	v_pk_mul_f32 v[112:113], v[134:135], v[154:155] op_sel_hi:[1,0]
	v_pk_mul_f32 v[114:115], v[132:133], v[154:155] op_sel_hi:[1,0]
	v_pk_fma_f32 v[112:113], v[118:119], v[152:153], v[112:113] op_sel_hi:[1,0,1] neg_lo:[0,0,1] neg_hi:[0,0,1]
	v_pk_fma_f32 v[114:115], v[116:117], v[152:153], v[114:115] op_sel_hi:[1,0,1] neg_lo:[0,0,1] neg_hi:[0,0,1]
	v_pk_add_f32 v[112:113], v[130:131], v[112:113]
	v_pk_add_f32 v[114:115], v[128:129], v[114:115]
	v_mul_f32_e32 v118, v112, v112
	v_mul_f32_e32 v116, v114, v114
	v_mul_f32_e32 v117, v115, v115
	v_mul_f32_e32 v119, v113, v113
	v_fmamk_f32 v116, v116, 0xbdd2d3e8, v124
	v_fmamk_f32 v117, v117, 0xbdd2d3e8, v124
	v_fmamk_f32 v118, v118, 0xbdd2d3e8, v124
	v_fmamk_f32 v119, v119, 0xbdd2d3e8, v124
	v_mul_f32_e32 v116, v114, v116
	v_mul_f32_e32 v117, v115, v117
	v_mul_f32_e32 v118, v112, v118
	v_mul_f32_e32 v119, v113, v119
	v_exp_f32_e32 v116, v116
	v_exp_f32_e32 v117, v117
	v_exp_f32_e32 v118, v118
	v_exp_f32_e32 v119, v119
	v_add_f32_e32 v116, 1.0, v116
	v_add_f32_e32 v117, 1.0, v117
	v_add_f32_e32 v118, 1.0, v118
	v_add_f32_e32 v119, 1.0, v119
	v_rcp_f32_e32 v116, v116
	v_rcp_f32_e32 v117, v117
	v_rcp_f32_e32 v118, v118
	v_rcp_f32_e32 v119, v119
	v_mul_f32_e32 v116, v114, v116
	v_mul_f32_e32 v117, v115, v117
	v_mul_f32_e32 v112, v112, v118
	v_mul_f32_e32 v113, v113, v119
	v_cvt_pk_f16_f32 v114, v122, v123
	v_cvt_pk_f16_f32 v115, v125, v126
	v_cvt_pk_f16_f32 v116, v116, v117
	v_cvt_pk_f16_f32 v117, v112, v113
	v_mad_i64_i32 v[112:113], s[2:3], v153, s0, 0
	v_lshlrev_b64 v[112:113], 1, v[112:113]
	v_lshl_add_u64 v[118:119], v[160:161], 0, v[112:113]
	global_store_dwordx4 v[118:119], v[114:117], off sc0 sc1
	s_nop 1
	v_pk_mul_f32 v[114:115], v[142:143], v[150:151] op_sel_hi:[1,0]
	v_pk_mul_f32 v[116:117], v[140:141], v[150:151] op_sel_hi:[1,0]
	v_pk_fma_f32 v[106:107], v[106:107], v[148:149], v[114:115] op_sel_hi:[1,0,1] neg_lo:[0,0,1] neg_hi:[0,0,1]
	v_pk_fma_f32 v[104:105], v[104:105], v[148:149], v[116:117] op_sel_hi:[1,0,1] neg_lo:[0,0,1] neg_hi:[0,0,1]
	v_pk_add_f32 v[106:107], v[138:139], v[106:107]
	v_pk_add_f32 v[104:105], v[136:137], v[104:105]
	v_mul_f32_e32 v116, v106, v106
	v_mul_f32_e32 v114, v104, v104
	v_mul_f32_e32 v115, v105, v105
	v_mul_f32_e32 v117, v107, v107
	v_fmamk_f32 v114, v114, 0xbdd2d3e8, v124
	v_fmamk_f32 v115, v115, 0xbdd2d3e8, v124
	v_fmamk_f32 v116, v116, 0xbdd2d3e8, v124
	v_fmamk_f32 v117, v117, 0xbdd2d3e8, v124
	v_mul_f32_e32 v114, v104, v114
	v_mul_f32_e32 v115, v105, v115
	v_mul_f32_e32 v116, v106, v116
	v_mul_f32_e32 v117, v107, v117
	v_exp_f32_e32 v114, v114
	v_exp_f32_e32 v115, v115
	v_exp_f32_e32 v116, v116
	v_exp_f32_e32 v117, v117
	v_add_f32_e32 v114, 1.0, v114
	v_add_f32_e32 v115, 1.0, v115
	v_add_f32_e32 v116, 1.0, v116
	v_add_f32_e32 v117, 1.0, v117
	v_rcp_f32_e32 v114, v114
	v_rcp_f32_e32 v115, v115
	v_rcp_f32_e32 v116, v116
	v_rcp_f32_e32 v117, v117
	v_mul_f32_e32 v114, v104, v114
	v_mul_f32_e32 v115, v105, v115
	v_mul_f32_e32 v116, v106, v116
	v_mul_f32_e32 v117, v107, v117
	v_pk_mul_f32 v[104:105], v[134:135], v[150:151] op_sel_hi:[1,0]
	v_pk_mul_f32 v[106:107], v[132:133], v[150:151] op_sel_hi:[1,0]
	v_pk_fma_f32 v[104:105], v[110:111], v[148:149], v[104:105] op_sel_hi:[1,0,1] neg_lo:[0,0,1] neg_hi:[0,0,1]
	v_pk_fma_f32 v[106:107], v[108:109], v[148:149], v[106:107] op_sel_hi:[1,0,1] neg_lo:[0,0,1] neg_hi:[0,0,1]
	v_pk_add_f32 v[104:105], v[130:131], v[104:105]
	v_pk_add_f32 v[106:107], v[128:129], v[106:107]
	v_mul_f32_e32 v110, v104, v104
	v_mul_f32_e32 v108, v106, v106
	v_mul_f32_e32 v109, v107, v107
	v_mul_f32_e32 v111, v105, v105
	v_fmamk_f32 v108, v108, 0xbdd2d3e8, v124
	v_fmamk_f32 v109, v109, 0xbdd2d3e8, v124
	v_fmamk_f32 v110, v110, 0xbdd2d3e8, v124
	v_fmamk_f32 v111, v111, 0xbdd2d3e8, v124
	v_mul_f32_e32 v108, v106, v108
	v_mul_f32_e32 v109, v107, v109
	v_mul_f32_e32 v110, v104, v110
	v_mul_f32_e32 v111, v105, v111
	v_exp_f32_e32 v108, v108
	v_exp_f32_e32 v109, v109
	v_exp_f32_e32 v110, v110
	v_exp_f32_e32 v111, v111
	v_add_f32_e32 v108, 1.0, v108
	v_add_f32_e32 v109, 1.0, v109
	v_add_f32_e32 v110, 1.0, v110
	v_add_f32_e32 v111, 1.0, v111
	v_rcp_f32_e32 v108, v108
	v_rcp_f32_e32 v109, v109
	v_rcp_f32_e32 v110, v110
	v_rcp_f32_e32 v111, v111
	v_mul_f32_e32 v108, v106, v108
	v_mul_f32_e32 v109, v107, v109
	v_mul_f32_e32 v104, v104, v110
	v_mul_f32_e32 v105, v105, v111
	v_cvt_pk_f16_f32 v106, v114, v115
	v_cvt_pk_f16_f32 v107, v116, v117
	v_cvt_pk_f16_f32 v108, v108, v109
	v_cvt_pk_f16_f32 v109, v104, v105
	v_mad_i64_i32 v[104:105], s[2:3], v155, s0, 0
	v_lshlrev_b64 v[104:105], 1, v[104:105]
	v_lshl_add_u64 v[110:111], v[160:161], 0, v[104:105]
	global_store_dwordx4 v[110:111], v[106:109], off sc0 sc1
	s_nop 1
	v_pk_mul_f32 v[106:107], v[142:143], v[146:147] op_sel_hi:[1,0]
	v_pk_mul_f32 v[108:109], v[140:141], v[146:147] op_sel_hi:[1,0]
	v_pk_fma_f32 v[98:99], v[98:99], v[144:145], v[106:107] op_sel_hi:[1,0,1] neg_lo:[0,0,1] neg_hi:[0,0,1]
	v_pk_fma_f32 v[96:97], v[96:97], v[144:145], v[108:109] op_sel_hi:[1,0,1] neg_lo:[0,0,1] neg_hi:[0,0,1]
	v_pk_add_f32 v[98:99], v[138:139], v[98:99]
	v_pk_add_f32 v[96:97], v[136:137], v[96:97]
	v_mul_f32_e32 v108, v98, v98
	v_mul_f32_e32 v106, v96, v96
	v_mul_f32_e32 v107, v97, v97
	v_mul_f32_e32 v109, v99, v99
	v_fmamk_f32 v106, v106, 0xbdd2d3e8, v124
	v_fmamk_f32 v107, v107, 0xbdd2d3e8, v124
	v_fmamk_f32 v108, v108, 0xbdd2d3e8, v124
	v_fmamk_f32 v109, v109, 0xbdd2d3e8, v124
	v_mul_f32_e32 v106, v96, v106
	v_mul_f32_e32 v107, v97, v107
	v_mul_f32_e32 v108, v98, v108
	v_mul_f32_e32 v109, v99, v109
	v_exp_f32_e32 v106, v106
	v_exp_f32_e32 v107, v107
	v_exp_f32_e32 v108, v108
	v_exp_f32_e32 v109, v109
	v_add_f32_e32 v106, 1.0, v106
	v_add_f32_e32 v107, 1.0, v107
	v_add_f32_e32 v108, 1.0, v108
	v_add_f32_e32 v109, 1.0, v109
	v_rcp_f32_e32 v106, v106
	v_rcp_f32_e32 v107, v107
	v_rcp_f32_e32 v108, v108
	v_rcp_f32_e32 v109, v109
	v_mul_f32_e32 v106, v96, v106
	v_mul_f32_e32 v107, v97, v107
	v_mul_f32_e32 v108, v98, v108
	v_mul_f32_e32 v109, v99, v109
	v_pk_mul_f32 v[96:97], v[134:135], v[146:147] op_sel_hi:[1,0]
	v_pk_mul_f32 v[98:99], v[132:133], v[146:147] op_sel_hi:[1,0]
	v_pk_fma_f32 v[96:97], v[102:103], v[144:145], v[96:97] op_sel_hi:[1,0,1] neg_lo:[0,0,1] neg_hi:[0,0,1]
	v_pk_fma_f32 v[98:99], v[100:101], v[144:145], v[98:99] op_sel_hi:[1,0,1] neg_lo:[0,0,1] neg_hi:[0,0,1]
	v_pk_add_f32 v[96:97], v[130:131], v[96:97]
	v_pk_add_f32 v[98:99], v[128:129], v[98:99]
	v_mul_f32_e32 v102, v96, v96
	v_mul_f32_e32 v100, v98, v98
	v_mul_f32_e32 v101, v99, v99
	v_mul_f32_e32 v103, v97, v97
	v_fmamk_f32 v100, v100, 0xbdd2d3e8, v124
	v_fmamk_f32 v101, v101, 0xbdd2d3e8, v124
	v_fmamk_f32 v102, v102, 0xbdd2d3e8, v124
	v_fmamk_f32 v103, v103, 0xbdd2d3e8, v124
	v_mul_f32_e32 v100, v98, v100
	v_mul_f32_e32 v101, v99, v101
	v_mul_f32_e32 v102, v96, v102
	v_mul_f32_e32 v103, v97, v103
	v_exp_f32_e32 v100, v100
	v_exp_f32_e32 v101, v101
	v_exp_f32_e32 v102, v102
	v_exp_f32_e32 v103, v103
	v_add_f32_e32 v100, 1.0, v100
	v_add_f32_e32 v101, 1.0, v101
	v_add_f32_e32 v102, 1.0, v102
	v_add_f32_e32 v103, 1.0, v103
	v_rcp_f32_e32 v100, v100
	v_rcp_f32_e32 v101, v101
	v_rcp_f32_e32 v102, v102
	v_rcp_f32_e32 v103, v103
	v_mul_f32_e32 v100, v98, v100
	v_mul_f32_e32 v101, v99, v101
	v_mul_f32_e32 v96, v96, v102
	v_mul_f32_e32 v97, v97, v103
	v_cvt_pk_f16_f32 v98, v106, v107
	v_cvt_pk_f16_f32 v99, v108, v109
	v_cvt_pk_f16_f32 v100, v100, v101
	v_cvt_pk_f16_f32 v101, v96, v97
	v_mad_i64_i32 v[96:97], s[0:1], v157, s0, 0
	v_lshlrev_b64 v[96:97], 1, v[96:97]
	v_lshl_add_u64 v[102:103], v[160:161], 0, v[96:97]
	global_store_dwordx4 v[102:103], v[98:101], off sc0 sc1
	v_pk_mul_f32 v[102:103], v[76:77], v[158:159] op_sel_hi:[1,0]
	s_nop 0
	v_pk_mul_f32 v[100:101], v[78:79], v[158:159] op_sel_hi:[1,0]
	v_pk_fma_f32 v[92:93], v[92:93], v[156:157], v[102:103] op_sel_hi:[1,0,1] neg_lo:[0,0,1] neg_hi:[0,0,1]
	v_pk_fma_f32 v[94:95], v[94:95], v[156:157], v[100:101] op_sel_hi:[1,0,1] neg_lo:[0,0,1] neg_hi:[0,0,1]
	v_pk_add_f32 v[92:93], v[72:73], v[92:93]
	v_pk_add_f32 v[94:95], v[74:75], v[94:95]
	v_mul_f32_e32 v100, v92, v92
	v_mul_f32_e32 v101, v93, v93
	v_mul_f32_e32 v102, v94, v94
	v_mul_f32_e32 v103, v95, v95
	v_fmamk_f32 v100, v100, 0xbdd2d3e8, v124
	v_fmamk_f32 v101, v101, 0xbdd2d3e8, v124
	v_fmamk_f32 v102, v102, 0xbdd2d3e8, v124
	v_fmamk_f32 v103, v103, 0xbdd2d3e8, v124
	v_mul_f32_e32 v100, v92, v100
	v_mul_f32_e32 v101, v93, v101
	v_mul_f32_e32 v102, v94, v102
	v_mul_f32_e32 v103, v95, v103
	v_exp_f32_e32 v100, v100
	v_exp_f32_e32 v101, v101
	v_exp_f32_e32 v102, v102
	v_exp_f32_e32 v103, v103
	v_add_f32_e32 v100, 1.0, v100
	v_add_f32_e32 v101, 1.0, v101
	v_add_f32_e32 v102, 1.0, v102
	v_add_f32_e32 v103, 1.0, v103
	v_rcp_f32_e32 v100, v100
	v_rcp_f32_e32 v101, v101
	v_rcp_f32_e32 v102, v102
	v_rcp_f32_e32 v103, v103
	v_mul_f32_e32 v100, v92, v100
	v_mul_f32_e32 v101, v93, v101
	v_mul_f32_e32 v102, v94, v102
	v_mul_f32_e32 v103, v95, v103
	v_pk_mul_f32 v[92:93], v[70:71], v[158:159] op_sel_hi:[1,0]
	v_pk_mul_f32 v[94:95], v[68:69], v[158:159] op_sel_hi:[1,0]
	v_pk_fma_f32 v[90:91], v[90:91], v[156:157], v[92:93] op_sel_hi:[1,0,1] neg_lo:[0,0,1] neg_hi:[0,0,1]
	v_pk_fma_f32 v[88:89], v[88:89], v[156:157], v[94:95] op_sel_hi:[1,0,1] neg_lo:[0,0,1] neg_hi:[0,0,1]
	v_pk_add_f32 v[90:91], v[34:35], v[90:91]
	v_pk_add_f32 v[88:89], v[32:33], v[88:89]
	v_mul_f32_e32 v95, v91, v91
	v_mul_f32_e32 v92, v88, v88
	v_mul_f32_e32 v93, v89, v89
	v_fmamk_f32 v92, v92, 0xbdd2d3e8, v124
	v_fmamk_f32 v93, v93, 0xbdd2d3e8, v124
	v_mul_f32_e32 v94, v90, v90
	v_fmamk_f32 v95, v95, 0xbdd2d3e8, v124
	v_mul_f32_e32 v92, v88, v92
	v_mul_f32_e32 v93, v89, v93
	v_fmamk_f32 v94, v94, 0xbdd2d3e8, v124
	v_mul_f32_e32 v95, v91, v95
	v_exp_f32_e32 v92, v92
	v_exp_f32_e32 v93, v93
	v_mul_f32_e32 v94, v90, v94
	v_exp_f32_e32 v95, v95
	v_exp_f32_e32 v94, v94
	v_add_f32_e32 v92, 1.0, v92
	v_add_f32_e32 v93, 1.0, v93
	v_add_f32_e32 v95, 1.0, v95
	v_rcp_f32_e32 v92, v92
	v_rcp_f32_e32 v93, v93
	v_add_f32_e32 v94, 1.0, v94
	v_rcp_f32_e32 v95, v95
	v_rcp_f32_e32 v94, v94
	v_lshl_add_u64 v[98:99], v[202:203], 1, s[6:7]
	v_mul_f32_e32 v92, v88, v92
	v_mul_f32_e32 v93, v89, v93
	v_mul_f32_e32 v91, v91, v95
	v_mul_f32_e32 v94, v90, v94
	v_cvt_pk_f16_f32 v88, v100, v101
	v_cvt_pk_f16_f32 v89, v102, v103
	v_cvt_pk_f16_f32 v90, v92, v93
	v_cvt_pk_f16_f32 v91, v94, v91
	v_lshl_add_u64 v[92:93], v[98:99], 0, v[120:121]
	global_store_dwordx4 v[92:93], v[88:91], off sc0 sc1
	s_nop 1
	v_pk_mul_f32 v[88:89], v[78:79], v[154:155] op_sel_hi:[1,0]
	v_pk_mul_f32 v[90:91], v[76:77], v[154:155] op_sel_hi:[1,0]
	v_pk_fma_f32 v[82:83], v[82:83], v[152:153], v[88:89] op_sel_hi:[1,0,1] neg_lo:[0,0,1] neg_hi:[0,0,1]
	v_pk_fma_f32 v[80:81], v[80:81], v[152:153], v[90:91] op_sel_hi:[1,0,1] neg_lo:[0,0,1] neg_hi:[0,0,1]
	v_pk_add_f32 v[82:83], v[74:75], v[82:83]
	v_pk_add_f32 v[80:81], v[72:73], v[80:81]
	v_mul_f32_e32 v90, v82, v82
	v_mul_f32_e32 v88, v80, v80
	v_mul_f32_e32 v89, v81, v81
	v_mul_f32_e32 v91, v83, v83
	v_fmamk_f32 v88, v88, 0xbdd2d3e8, v124
	v_fmamk_f32 v89, v89, 0xbdd2d3e8, v124
	v_fmamk_f32 v90, v90, 0xbdd2d3e8, v124
	v_fmamk_f32 v91, v91, 0xbdd2d3e8, v124
	v_mul_f32_e32 v88, v80, v88
	v_mul_f32_e32 v89, v81, v89
	v_mul_f32_e32 v90, v82, v90
	v_mul_f32_e32 v91, v83, v91
	v_exp_f32_e32 v88, v88
	v_exp_f32_e32 v89, v89
	v_exp_f32_e32 v90, v90
	v_exp_f32_e32 v91, v91
	v_add_f32_e32 v88, 1.0, v88
	v_add_f32_e32 v89, 1.0, v89
	v_add_f32_e32 v90, 1.0, v90
	v_add_f32_e32 v91, 1.0, v91
	v_rcp_f32_e32 v88, v88
	v_rcp_f32_e32 v89, v89
	v_rcp_f32_e32 v90, v90
	v_rcp_f32_e32 v91, v91
	v_mul_f32_e32 v88, v80, v88
	v_mul_f32_e32 v89, v81, v89
	v_mul_f32_e32 v90, v82, v90
	v_mul_f32_e32 v91, v83, v91
	v_pk_mul_f32 v[80:81], v[70:71], v[154:155] op_sel_hi:[1,0]
	v_pk_mul_f32 v[82:83], v[68:69], v[154:155] op_sel_hi:[1,0]
	v_pk_fma_f32 v[80:81], v[86:87], v[152:153], v[80:81] op_sel_hi:[1,0,1] neg_lo:[0,0,1] neg_hi:[0,0,1]
	v_pk_fma_f32 v[82:83], v[84:85], v[152:153], v[82:83] op_sel_hi:[1,0,1] neg_lo:[0,0,1] neg_hi:[0,0,1]
	v_pk_add_f32 v[80:81], v[34:35], v[80:81]
	v_pk_add_f32 v[82:83], v[32:33], v[82:83]
	v_mul_f32_e32 v86, v80, v80
	v_mul_f32_e32 v84, v82, v82
	v_mul_f32_e32 v85, v83, v83
	v_mul_f32_e32 v87, v81, v81
	v_fmamk_f32 v84, v84, 0xbdd2d3e8, v124
	v_fmamk_f32 v85, v85, 0xbdd2d3e8, v124
	v_fmamk_f32 v86, v86, 0xbdd2d3e8, v124
	v_fmamk_f32 v87, v87, 0xbdd2d3e8, v124
	v_mul_f32_e32 v84, v82, v84
	v_mul_f32_e32 v85, v83, v85
	v_mul_f32_e32 v86, v80, v86
	v_mul_f32_e32 v87, v81, v87
	v_exp_f32_e32 v84, v84
	v_exp_f32_e32 v85, v85
	v_exp_f32_e32 v86, v86
	v_exp_f32_e32 v87, v87
	v_add_f32_e32 v84, 1.0, v84
	v_add_f32_e32 v85, 1.0, v85
	v_add_f32_e32 v86, 1.0, v86
	v_add_f32_e32 v87, 1.0, v87
	v_rcp_f32_e32 v84, v84
	v_rcp_f32_e32 v85, v85
	v_rcp_f32_e32 v86, v86
	v_rcp_f32_e32 v87, v87
	v_mul_f32_e32 v82, v82, v84
	v_mul_f32_e32 v83, v83, v85
	v_mul_f32_e32 v84, v80, v86
	v_mul_f32_e32 v85, v81, v87
	v_cvt_pk_f16_f32 v80, v88, v89
	v_cvt_pk_f16_f32 v81, v90, v91
	v_cvt_pk_f16_f32 v82, v82, v83
	v_cvt_pk_f16_f32 v83, v84, v85
	v_lshl_add_u64 v[84:85], v[98:99], 0, v[112:113]
	global_store_dwordx4 v[84:85], v[80:83], off sc0 sc1
	s_nop 1
	v_pk_mul_f32 v[80:81], v[78:79], v[150:151] op_sel_hi:[1,0]
	v_pk_mul_f32 v[82:83], v[76:77], v[150:151] op_sel_hi:[1,0]
	v_pk_fma_f32 v[62:63], v[62:63], v[148:149], v[80:81] op_sel_hi:[1,0,1] neg_lo:[0,0,1] neg_hi:[0,0,1]
	v_pk_fma_f32 v[60:61], v[60:61], v[148:149], v[82:83] op_sel_hi:[1,0,1] neg_lo:[0,0,1] neg_hi:[0,0,1]
	v_pk_add_f32 v[62:63], v[74:75], v[62:63]
	v_pk_add_f32 v[60:61], v[72:73], v[60:61]
	v_mul_f32_e32 v82, v62, v62
	v_mul_f32_e32 v80, v60, v60
	v_mul_f32_e32 v81, v61, v61
	v_mul_f32_e32 v83, v63, v63
	v_fmamk_f32 v80, v80, 0xbdd2d3e8, v124
	v_fmamk_f32 v81, v81, 0xbdd2d3e8, v124
	v_fmamk_f32 v82, v82, 0xbdd2d3e8, v124
	v_fmamk_f32 v83, v83, 0xbdd2d3e8, v124
	v_mul_f32_e32 v80, v60, v80
	v_mul_f32_e32 v81, v61, v81
	v_mul_f32_e32 v82, v62, v82
	v_mul_f32_e32 v83, v63, v83
	v_exp_f32_e32 v80, v80
	v_exp_f32_e32 v81, v81
	v_exp_f32_e32 v82, v82
	v_exp_f32_e32 v83, v83
	v_add_f32_e32 v80, 1.0, v80
	v_add_f32_e32 v81, 1.0, v81
	v_add_f32_e32 v82, 1.0, v82
	v_add_f32_e32 v83, 1.0, v83
	v_rcp_f32_e32 v80, v80
	v_rcp_f32_e32 v81, v81
	v_rcp_f32_e32 v82, v82
	v_rcp_f32_e32 v83, v83
	v_mul_f32_e32 v80, v60, v80
	v_mul_f32_e32 v81, v61, v81
	v_mul_f32_e32 v82, v62, v82
	v_mul_f32_e32 v83, v63, v83
	v_pk_mul_f32 v[60:61], v[70:71], v[150:151] op_sel_hi:[1,0]
	v_pk_mul_f32 v[62:63], v[68:69], v[150:151] op_sel_hi:[1,0]
	v_pk_fma_f32 v[60:61], v[66:67], v[148:149], v[60:61] op_sel_hi:[1,0,1] neg_lo:[0,0,1] neg_hi:[0,0,1]
	v_pk_fma_f32 v[62:63], v[64:65], v[148:149], v[62:63] op_sel_hi:[1,0,1] neg_lo:[0,0,1] neg_hi:[0,0,1]
	v_pk_add_f32 v[60:61], v[34:35], v[60:61]
	v_pk_add_f32 v[62:63], v[32:33], v[62:63]
	v_mul_f32_e32 v66, v60, v60
	v_mul_f32_e32 v64, v62, v62
	v_mul_f32_e32 v65, v63, v63
	v_mul_f32_e32 v67, v61, v61
	v_fmamk_f32 v64, v64, 0xbdd2d3e8, v124
	v_fmamk_f32 v65, v65, 0xbdd2d3e8, v124
	v_fmamk_f32 v66, v66, 0xbdd2d3e8, v124
	v_fmamk_f32 v67, v67, 0xbdd2d3e8, v124
	v_mul_f32_e32 v64, v62, v64
	v_mul_f32_e32 v65, v63, v65
	v_mul_f32_e32 v66, v60, v66
	v_mul_f32_e32 v67, v61, v67
	v_exp_f32_e32 v64, v64
	v_exp_f32_e32 v65, v65
	v_exp_f32_e32 v66, v66
	v_exp_f32_e32 v67, v67
	v_add_f32_e32 v64, 1.0, v64
	v_add_f32_e32 v65, 1.0, v65
	v_add_f32_e32 v66, 1.0, v66
	v_add_f32_e32 v67, 1.0, v67
	v_rcp_f32_e32 v64, v64
	v_rcp_f32_e32 v65, v65
	v_rcp_f32_e32 v66, v66
	v_rcp_f32_e32 v67, v67
	v_mul_f32_e32 v62, v62, v64
	v_mul_f32_e32 v63, v63, v65
	v_mul_f32_e32 v64, v60, v66
	v_mul_f32_e32 v65, v61, v67
	v_cvt_pk_f16_f32 v60, v80, v81
	v_cvt_pk_f16_f32 v61, v82, v83
	v_cvt_pk_f16_f32 v62, v62, v63
	v_cvt_pk_f16_f32 v63, v64, v65
	v_lshl_add_u64 v[64:65], v[98:99], 0, v[104:105]
	global_store_dwordx4 v[64:65], v[60:63], off sc0 sc1
	s_nop 1
	v_pk_mul_f32 v[60:61], v[78:79], v[146:147] op_sel_hi:[1,0]
	v_pk_mul_f32 v[62:63], v[76:77], v[146:147] op_sel_hi:[1,0]
	v_pk_fma_f32 v[54:55], v[54:55], v[144:145], v[60:61] op_sel_hi:[1,0,1] neg_lo:[0,0,1] neg_hi:[0,0,1]
	v_pk_fma_f32 v[52:53], v[52:53], v[144:145], v[62:63] op_sel_hi:[1,0,1] neg_lo:[0,0,1] neg_hi:[0,0,1]
	v_pk_add_f32 v[54:55], v[74:75], v[54:55]
	v_pk_add_f32 v[52:53], v[72:73], v[52:53]
	v_mul_f32_e32 v62, v54, v54
	v_mul_f32_e32 v63, v55, v55
	v_fmamk_f32 v62, v62, 0xbdd2d3e8, v124
	v_fmamk_f32 v63, v63, 0xbdd2d3e8, v124
	v_mul_f32_e32 v62, v54, v62
	v_mul_f32_e32 v63, v55, v63
	v_exp_f32_e32 v62, v62
	v_exp_f32_e32 v63, v63
	v_mul_f32_e32 v60, v52, v52
	v_mul_f32_e32 v61, v53, v53
	v_add_f32_e32 v62, 1.0, v62
	v_add_f32_e32 v63, 1.0, v63
	v_fmamk_f32 v60, v60, 0xbdd2d3e8, v124
	v_fmamk_f32 v61, v61, 0xbdd2d3e8, v124
	v_rcp_f32_e32 v62, v62
	v_rcp_f32_e32 v63, v63
	v_mul_f32_e32 v60, v52, v60
	v_mul_f32_e32 v61, v53, v61
	v_exp_f32_e32 v60, v60
	v_exp_f32_e32 v61, v61
	v_mul_f32_e32 v62, v54, v62
	v_mul_f32_e32 v63, v55, v63
	v_pk_mul_f32 v[54:55], v[68:69], v[146:147] op_sel_hi:[1,0]
	v_add_f32_e32 v60, 1.0, v60
	v_pk_fma_f32 v[54:55], v[56:57], v[144:145], v[54:55] op_sel_hi:[1,0,1] neg_lo:[0,0,1] neg_hi:[0,0,1]
	v_add_f32_e32 v61, 1.0, v61
	v_pk_add_f32 v[32:33], v[32:33], v[54:55]
	v_rcp_f32_e32 v60, v60
	v_rcp_f32_e32 v61, v61
	v_mul_f32_e32 v55, v33, v33
	v_mul_f32_e32 v54, v32, v32
	v_fmamk_f32 v55, v55, 0xbdd2d3e8, v124
	v_fmamk_f32 v54, v54, 0xbdd2d3e8, v124
	v_mul_f32_e32 v55, v33, v55
	v_mul_f32_e32 v54, v32, v54
	v_exp_f32_e32 v55, v55
	v_mul_f32_e32 v60, v52, v60
	v_mul_f32_e32 v61, v53, v61
	v_pk_mul_f32 v[52:53], v[70:71], v[146:147] op_sel_hi:[1,0]
	v_exp_f32_e32 v54, v54
	v_pk_fma_f32 v[52:53], v[58:59], v[144:145], v[52:53] op_sel_hi:[1,0,1] neg_lo:[0,0,1] neg_hi:[0,0,1]
	s_nop 0
	v_pk_add_f32 v[34:35], v[34:35], v[52:53]
	v_add_f32_e32 v53, 1.0, v55
	v_mul_f32_e32 v55, v35, v35
	v_add_f32_e32 v52, 1.0, v54
	v_mul_f32_e32 v54, v34, v34
	v_fmamk_f32 v55, v55, 0xbdd2d3e8, v124
	v_fmamk_f32 v54, v54, 0xbdd2d3e8, v124
	v_mul_f32_e32 v55, v35, v55
	v_mul_f32_e32 v54, v34, v54
	v_exp_f32_e32 v55, v55
	v_exp_f32_e32 v54, v54
	v_rcp_f32_e32 v52, v52
	v_rcp_f32_e32 v53, v53
	v_add_f32_e32 v55, 1.0, v55
	v_add_f32_e32 v54, 1.0, v54
	v_rcp_f32_e32 v55, v55
	v_rcp_f32_e32 v54, v54
	v_mul_f32_e32 v52, v32, v52
	v_mul_f32_e32 v53, v33, v53
	v_mul_f32_e32 v35, v35, v55
	v_mul_f32_e32 v54, v34, v54
	v_cvt_pk_f16_f32 v32, v60, v61
	v_cvt_pk_f16_f32 v33, v62, v63
	v_cvt_pk_f16_f32 v34, v52, v53
	v_cvt_pk_f16_f32 v35, v54, v35
	v_lshl_add_u64 v[52:53], v[98:99], 0, v[96:97]
	global_store_dwordx4 v[52:53], v[32:35], off sc0 sc1
	v_pk_mul_f32 v[52:53], v[12:13], v[158:159] op_sel_hi:[1,0]
	s_nop 0
	v_pk_mul_f32 v[34:35], v[14:15], v[158:159] op_sel_hi:[1,0]
	v_pk_fma_f32 v[48:49], v[48:49], v[156:157], v[52:53] op_sel_hi:[1,0,1] neg_lo:[0,0,1] neg_hi:[0,0,1]
	v_pk_fma_f32 v[34:35], v[50:51], v[156:157], v[34:35] op_sel_hi:[1,0,1] neg_lo:[0,0,1] neg_hi:[0,0,1]
	v_pk_add_f32 v[48:49], v[8:9], v[48:49]
	v_pk_add_f32 v[34:35], v[10:11], v[34:35]
	v_mul_f32_e32 v50, v48, v48
	v_mul_f32_e32 v51, v49, v49
	v_mul_f32_e32 v52, v34, v34
	v_mul_f32_e32 v53, v35, v35
	v_fmamk_f32 v50, v50, 0xbdd2d3e8, v124
	v_fmamk_f32 v51, v51, 0xbdd2d3e8, v124
	v_fmamk_f32 v52, v52, 0xbdd2d3e8, v124
	v_fmamk_f32 v53, v53, 0xbdd2d3e8, v124
	v_mul_f32_e32 v50, v48, v50
	v_mul_f32_e32 v51, v49, v51
	v_mul_f32_e32 v52, v34, v52
	v_mul_f32_e32 v53, v35, v53
	v_exp_f32_e32 v50, v50
	v_exp_f32_e32 v51, v51
	v_exp_f32_e32 v52, v52
	v_exp_f32_e32 v53, v53
	v_add_f32_e32 v50, 1.0, v50
	v_add_f32_e32 v51, 1.0, v51
	v_add_f32_e32 v52, 1.0, v52
	v_add_f32_e32 v53, 1.0, v53
	v_rcp_f32_e32 v50, v50
	v_rcp_f32_e32 v51, v51
	v_rcp_f32_e32 v52, v52
	v_rcp_f32_e32 v53, v53
	v_mul_f32_e32 v50, v48, v50
	v_mul_f32_e32 v51, v49, v51
	v_mul_f32_e32 v52, v34, v52
	v_mul_f32_e32 v53, v35, v53
	v_pk_mul_f32 v[34:35], v[6:7], v[158:159] op_sel_hi:[1,0]
	v_pk_mul_f32 v[48:49], v[4:5], v[158:159] op_sel_hi:[1,0]
	v_pk_fma_f32 v[34:35], v[46:47], v[156:157], v[34:35] op_sel_hi:[1,0,1] neg_lo:[0,0,1] neg_hi:[0,0,1]
	v_pk_fma_f32 v[44:45], v[44:45], v[156:157], v[48:49] op_sel_hi:[1,0,1] neg_lo:[0,0,1] neg_hi:[0,0,1]
	v_pk_add_f32 v[34:35], v[2:3], v[34:35]
	v_pk_add_f32 v[44:45], v[0:1], v[44:45]
	v_mul_f32_e32 v48, v34, v34
	v_mul_f32_e32 v46, v44, v44
	v_mul_f32_e32 v47, v45, v45
	v_mul_f32_e32 v49, v35, v35
	v_fmamk_f32 v46, v46, 0xbdd2d3e8, v124
	v_fmamk_f32 v47, v47, 0xbdd2d3e8, v124
	v_fmamk_f32 v48, v48, 0xbdd2d3e8, v124
	v_fmamk_f32 v49, v49, 0xbdd2d3e8, v124
	v_mul_f32_e32 v46, v44, v46
	v_mul_f32_e32 v47, v45, v47
	v_mul_f32_e32 v48, v34, v48
	v_mul_f32_e32 v49, v35, v49
	v_exp_f32_e32 v46, v46
	v_exp_f32_e32 v47, v47
	v_exp_f32_e32 v48, v48
	v_exp_f32_e32 v49, v49
	v_add_f32_e32 v46, 1.0, v46
	v_add_f32_e32 v47, 1.0, v47
	v_add_f32_e32 v48, 1.0, v48
	v_add_f32_e32 v49, 1.0, v49
	v_rcp_f32_e32 v46, v46
	v_rcp_f32_e32 v47, v47
	v_rcp_f32_e32 v48, v48
	v_rcp_f32_e32 v49, v49
	v_lshl_add_u64 v[32:33], v[200:201], 1, s[6:7]
	v_mul_f32_e32 v46, v44, v46
	v_mul_f32_e32 v47, v45, v47
	v_mul_f32_e32 v34, v34, v48
	v_mul_f32_e32 v35, v35, v49
	v_cvt_pk_f16_f32 v44, v50, v51
	v_cvt_pk_f16_f32 v45, v52, v53
	v_cvt_pk_f16_f32 v46, v46, v47
	v_cvt_pk_f16_f32 v47, v34, v35
	v_lshl_add_u64 v[34:35], v[32:33], 0, v[120:121]
	global_store_dwordx4 v[34:35], v[44:47], off sc0 sc1
	v_pk_mul_f32 v[34:35], v[14:15], v[154:155] op_sel_hi:[1,0]
	s_nop 0
	v_pk_mul_f32 v[44:45], v[12:13], v[154:155] op_sel_hi:[1,0]
	v_pk_fma_f32 v[34:35], v[38:39], v[152:153], v[34:35] op_sel_hi:[1,0,1] neg_lo:[0,0,1] neg_hi:[0,0,1]
	v_pk_fma_f32 v[36:37], v[36:37], v[152:153], v[44:45] op_sel_hi:[1,0,1] neg_lo:[0,0,1] neg_hi:[0,0,1]
	v_pk_add_f32 v[34:35], v[10:11], v[34:35]
	v_pk_add_f32 v[36:37], v[8:9], v[36:37]
	v_mul_f32_e32 v44, v34, v34
	v_mul_f32_e32 v38, v36, v36
	v_mul_f32_e32 v39, v37, v37
	v_fmamk_f32 v38, v38, 0xbdd2d3e8, v124
	v_fmamk_f32 v39, v39, 0xbdd2d3e8, v124
	v_mul_f32_e32 v45, v35, v35
	v_mul_f32_e32 v38, v36, v38
	v_mul_f32_e32 v39, v37, v39
	v_fmamk_f32 v44, v44, 0xbdd2d3e8, v124
	v_fmamk_f32 v45, v45, 0xbdd2d3e8, v124
	v_exp_f32_e32 v38, v38
	v_exp_f32_e32 v39, v39
	v_mul_f32_e32 v44, v34, v44
	v_mul_f32_e32 v45, v35, v45
	v_exp_f32_e32 v44, v44
	v_exp_f32_e32 v45, v45
	v_add_f32_e32 v38, 1.0, v38
	v_add_f32_e32 v39, 1.0, v39
	v_rcp_f32_e32 v38, v38
	v_rcp_f32_e32 v39, v39
	v_add_f32_e32 v44, 1.0, v44
	v_add_f32_e32 v45, 1.0, v45
	v_rcp_f32_e32 v44, v44
	v_rcp_f32_e32 v45, v45
	v_mul_f32_e32 v38, v36, v38
	v_mul_f32_e32 v39, v37, v39
	v_pk_mul_f32 v[36:37], v[4:5], v[154:155] op_sel_hi:[1,0]
	v_mul_f32_e32 v44, v34, v44
	v_mul_f32_e32 v45, v35, v45
	v_pk_mul_f32 v[34:35], v[6:7], v[154:155] op_sel_hi:[1,0]
	v_pk_fma_f32 v[36:37], v[40:41], v[152:153], v[36:37] op_sel_hi:[1,0,1] neg_lo:[0,0,1] neg_hi:[0,0,1]
	v_pk_fma_f32 v[34:35], v[42:43], v[152:153], v[34:35] op_sel_hi:[1,0,1] neg_lo:[0,0,1] neg_hi:[0,0,1]
	v_pk_add_f32 v[36:37], v[0:1], v[36:37]
	v_pk_add_f32 v[34:35], v[2:3], v[34:35]
	v_mul_f32_e32 v40, v36, v36
	v_mul_f32_e32 v41, v37, v37
	v_fmamk_f32 v40, v40, 0xbdd2d3e8, v124
	v_fmamk_f32 v41, v41, 0xbdd2d3e8, v124
	v_mul_f32_e32 v42, v34, v34
	v_mul_f32_e32 v43, v35, v35
	v_mul_f32_e32 v40, v36, v40
	v_mul_f32_e32 v41, v37, v41
	v_fmamk_f32 v42, v42, 0xbdd2d3e8, v124
	v_fmamk_f32 v43, v43, 0xbdd2d3e8, v124
	v_exp_f32_e32 v40, v40
	v_exp_f32_e32 v41, v41
	v_mul_f32_e32 v42, v34, v42
	v_mul_f32_e32 v43, v35, v43
	v_exp_f32_e32 v42, v42
	v_exp_f32_e32 v43, v43
	v_add_f32_e32 v40, 1.0, v40
	v_add_f32_e32 v41, 1.0, v41
	v_rcp_f32_e32 v40, v40
	v_rcp_f32_e32 v41, v41
	v_add_f32_e32 v42, 1.0, v42
	v_add_f32_e32 v43, 1.0, v43
	v_rcp_f32_e32 v42, v42
	v_rcp_f32_e32 v43, v43
	v_mul_f32_e32 v36, v36, v40
	v_mul_f32_e32 v37, v37, v41
	v_mul_f32_e32 v40, v34, v42
	v_mul_f32_e32 v41, v35, v43
	v_cvt_pk_f16_f32 v34, v38, v39
	v_cvt_pk_f16_f32 v35, v44, v45
	v_cvt_pk_f16_f32 v36, v36, v37
	v_cvt_pk_f16_f32 v37, v40, v41
	v_lshl_add_u64 v[38:39], v[32:33], 0, v[112:113]
	global_store_dwordx4 v[38:39], v[34:37], off sc0 sc1
	s_nop 1
	v_pk_mul_f32 v[34:35], v[14:15], v[150:151] op_sel_hi:[1,0]
	v_pk_mul_f32 v[36:37], v[12:13], v[150:151] op_sel_hi:[1,0]
	v_pk_fma_f32 v[26:27], v[26:27], v[148:149], v[34:35] op_sel_hi:[1,0,1] neg_lo:[0,0,1] neg_hi:[0,0,1]
	v_pk_fma_f32 v[24:25], v[24:25], v[148:149], v[36:37] op_sel_hi:[1,0,1] neg_lo:[0,0,1] neg_hi:[0,0,1]
	v_pk_add_f32 v[26:27], v[10:11], v[26:27]
	v_pk_add_f32 v[24:25], v[8:9], v[24:25]
	v_mul_f32_e32 v36, v26, v26
	v_mul_f32_e32 v34, v24, v24
	v_mul_f32_e32 v35, v25, v25
	v_mul_f32_e32 v37, v27, v27
	v_fmamk_f32 v34, v34, 0xbdd2d3e8, v124
	v_fmamk_f32 v35, v35, 0xbdd2d3e8, v124
	v_fmamk_f32 v36, v36, 0xbdd2d3e8, v124
	v_fmamk_f32 v37, v37, 0xbdd2d3e8, v124
	v_mul_f32_e32 v34, v24, v34
	v_mul_f32_e32 v35, v25, v35
	v_mul_f32_e32 v36, v26, v36
	v_mul_f32_e32 v37, v27, v37
	v_exp_f32_e32 v34, v34
	v_exp_f32_e32 v35, v35
	v_exp_f32_e32 v36, v36
	v_exp_f32_e32 v37, v37
	v_add_f32_e32 v34, 1.0, v34
	v_add_f32_e32 v35, 1.0, v35
	v_add_f32_e32 v36, 1.0, v36
	v_add_f32_e32 v37, 1.0, v37
	v_rcp_f32_e32 v34, v34
	v_rcp_f32_e32 v35, v35
	v_rcp_f32_e32 v36, v36
	v_rcp_f32_e32 v37, v37
	v_mul_f32_e32 v34, v24, v34
	v_mul_f32_e32 v35, v25, v35
	v_mul_f32_e32 v36, v26, v36
	v_mul_f32_e32 v37, v27, v37
	v_pk_mul_f32 v[24:25], v[6:7], v[150:151] op_sel_hi:[1,0]
	v_pk_mul_f32 v[26:27], v[4:5], v[150:151] op_sel_hi:[1,0]
	v_pk_fma_f32 v[24:25], v[30:31], v[148:149], v[24:25] op_sel_hi:[1,0,1] neg_lo:[0,0,1] neg_hi:[0,0,1]
	v_pk_fma_f32 v[26:27], v[28:29], v[148:149], v[26:27] op_sel_hi:[1,0,1] neg_lo:[0,0,1] neg_hi:[0,0,1]
	v_pk_mul_f32 v[4:5], v[4:5], v[146:147] op_sel_hi:[1,0]
	v_pk_add_f32 v[26:27], v[0:1], v[26:27]
	v_pk_add_f32 v[24:25], v[2:3], v[24:25]
	v_pk_mul_f32 v[14:15], v[14:15], v[146:147] op_sel_hi:[1,0]
	v_pk_mul_f32 v[12:13], v[12:13], v[146:147] op_sel_hi:[1,0]
	v_pk_mul_f32 v[6:7], v[6:7], v[146:147] op_sel_hi:[1,0]
	v_pk_fma_f32 v[4:5], v[20:21], v[144:145], v[4:5] op_sel_hi:[1,0,1] neg_lo:[0,0,1] neg_hi:[0,0,1]
	v_mul_f32_e32 v28, v26, v26
	v_mul_f32_e32 v29, v27, v27
	v_mul_f32_e32 v30, v24, v24
	v_mul_f32_e32 v31, v25, v25
	v_pk_fma_f32 v[12:13], v[16:17], v[144:145], v[12:13] op_sel_hi:[1,0,1] neg_lo:[0,0,1] neg_hi:[0,0,1]
	v_pk_fma_f32 v[14:15], v[18:19], v[144:145], v[14:15] op_sel_hi:[1,0,1] neg_lo:[0,0,1] neg_hi:[0,0,1]
	v_pk_fma_f32 v[6:7], v[22:23], v[144:145], v[6:7] op_sel_hi:[1,0,1] neg_lo:[0,0,1] neg_hi:[0,0,1]
	v_pk_add_f32 v[0:1], v[0:1], v[4:5]
	v_fmamk_f32 v28, v28, 0xbdd2d3e8, v124
	v_fmamk_f32 v29, v29, 0xbdd2d3e8, v124
	v_fmamk_f32 v30, v30, 0xbdd2d3e8, v124
	v_fmamk_f32 v31, v31, 0xbdd2d3e8, v124
	v_pk_add_f32 v[8:9], v[8:9], v[12:13]
	v_pk_add_f32 v[10:11], v[10:11], v[14:15]
	v_mul_f32_e32 v4, v0, v0
	v_mul_f32_e32 v5, v1, v1
	v_pk_add_f32 v[2:3], v[2:3], v[6:7]
	v_mul_f32_e32 v28, v26, v28
	v_mul_f32_e32 v29, v27, v29
	v_mul_f32_e32 v30, v24, v30
	v_mul_f32_e32 v31, v25, v31
	v_mul_f32_e32 v12, v8, v8
	v_mul_f32_e32 v13, v9, v9
	v_mul_f32_e32 v14, v10, v10
	v_mul_f32_e32 v15, v11, v11
	v_fmamk_f32 v4, v4, 0xbdd2d3e8, v124
	v_fmamk_f32 v5, v5, 0xbdd2d3e8, v124
	v_mul_f32_e32 v6, v2, v2
	v_mul_f32_e32 v7, v3, v3
	v_exp_f32_e32 v28, v28
	v_exp_f32_e32 v29, v29
	v_exp_f32_e32 v30, v30
	v_exp_f32_e32 v31, v31
	v_fmamk_f32 v12, v12, 0xbdd2d3e8, v124
	v_fmamk_f32 v13, v13, 0xbdd2d3e8, v124
	v_fmamk_f32 v14, v14, 0xbdd2d3e8, v124
	v_fmamk_f32 v15, v15, 0xbdd2d3e8, v124
	v_mul_f32_e32 v4, v0, v4
	v_mul_f32_e32 v5, v1, v5
	v_fmamk_f32 v6, v6, 0xbdd2d3e8, v124
	v_fmac_f32_e32 v124, 0xbdd2d3e8, v7
	v_mul_f32_e32 v12, v8, v12
	v_mul_f32_e32 v13, v9, v13
	v_mul_f32_e32 v14, v10, v14
	v_mul_f32_e32 v15, v11, v15
	v_exp_f32_e32 v4, v4
	v_exp_f32_e32 v5, v5
	v_mul_f32_e32 v6, v2, v6
	v_mul_f32_e32 v7, v3, v124
	v_exp_f32_e32 v12, v12
	v_exp_f32_e32 v13, v13
	v_exp_f32_e32 v14, v14
	v_exp_f32_e32 v15, v15
	v_exp_f32_e32 v6, v6
	v_exp_f32_e32 v7, v7
	v_add_f32_e32 v28, 1.0, v28
	v_add_f32_e32 v29, 1.0, v29
	v_add_f32_e32 v30, 1.0, v30
	v_add_f32_e32 v31, 1.0, v31
	v_rcp_f32_e32 v28, v28
	v_rcp_f32_e32 v29, v29
	v_rcp_f32_e32 v30, v30
	v_rcp_f32_e32 v31, v31
	v_add_f32_e32 v4, 1.0, v4
	v_add_f32_e32 v5, 1.0, v5
	v_add_f32_e32 v12, 1.0, v12
	v_add_f32_e32 v13, 1.0, v13
	v_add_f32_e32 v14, 1.0, v14
	v_add_f32_e32 v15, 1.0, v15
	v_rcp_f32_e32 v4, v4
	v_rcp_f32_e32 v5, v5
	v_add_f32_e32 v6, 1.0, v6
	v_add_f32_e32 v7, 1.0, v7
	v_rcp_f32_e32 v12, v12
	v_rcp_f32_e32 v13, v13
	v_rcp_f32_e32 v14, v14
	v_rcp_f32_e32 v15, v15
	v_rcp_f32_e32 v6, v6
	v_rcp_f32_e32 v7, v7
	v_mul_f32_e32 v26, v26, v28
	v_mul_f32_e32 v27, v27, v29
	v_mul_f32_e32 v28, v24, v30
	v_mul_f32_e32 v29, v25, v31
	v_cvt_pk_f16_f32 v24, v34, v35
	v_cvt_pk_f16_f32 v25, v36, v37
	v_cvt_pk_f16_f32 v26, v26, v27
	v_cvt_pk_f16_f32 v27, v28, v29
	v_lshl_add_u64 v[28:29], v[32:33], 0, v[104:105]
	v_mul_f32_e32 v4, v0, v4
	v_mul_f32_e32 v5, v1, v5
	global_store_dwordx4 v[28:29], v[24:27], off sc0 sc1
	v_mul_f32_e32 v8, v8, v12
	v_mul_f32_e32 v9, v9, v13
	v_mul_f32_e32 v10, v10, v14
	v_mul_f32_e32 v11, v11, v15
	v_mul_f32_e32 v6, v2, v6
	v_mul_f32_e32 v3, v3, v7
	v_cvt_pk_f16_f32 v0, v8, v9
	v_cvt_pk_f16_f32 v1, v10, v11
	v_cvt_pk_f16_f32 v2, v4, v5
	v_lshl_add_u64 v[4:5], v[32:33], 0, v[96:97]
	v_cvt_pk_f16_f32 v3, v6, v3
	global_store_dwordx4 v[4:5], v[0:3], off sc0 sc1
	s_endpgm
	.p2align	8
